# grid barriers 2..13: L1 invalidate (buffer_inv sc1) issued right after the arrival atomic, overlapping its round trip, instead of after the release is observed
# speedup vs baseline: 1.0367x; 1.0367x over previous
; __device__ __forceinline__ unsigned xb_ld(unsigned* p)              { return __hip_atomic_load(p, __ATOMIC_RELAXED, __HIP_MEMORY_SCOPE_AGENT); }
; __device__ __forceinline__ unsigned xb_add(unsigned* p, unsigned v) { return __hip_atomic_fetch_add(p, v, __ATOMIC_RELAXED, __HIP_MEMORY_SCOPE_AGENT); }
; #define XB_SPIN(cond, bar) do { unsigned _sp = 0; while (cond) { __builtin_amdgcn_s_sleep(1); \
;     if ((++_sp & 255u) == 0u) { if (xb_ld(&(bar)[XB_TMO])) break; if (_sp > XB_SPIN_CAP) { atomicAdd(&(bar)[XB_TMO], 1u); break; } } } } while (0)
; __device__ __forceinline__ void xcd_barrier(const XcdBarrier& b) {
;   asm volatile("s_waitcnt vmcnt(0)" ::: "memory");
;   __syncthreads();
;   if (threadIdx.x == 0) {
;     unsigned* bar = b.bar;
;     __builtin_amdgcn_s_waitcnt(0);
;     unsigned nloc = b.st[0], nx = b.st[1];
;     if (nloc == 0u) { xcd_barrier_complete(bar, b.x, nloc, nx); b.st[0] = nloc; b.st[1] = nx; }
;     const unsigned old = xb_add(&bar[XB_XSUB(b.x)], 1u);
;     const unsigned gen = old / nloc;
;     if (old + 1u == (gen + 1u) * nloc) {
;       __builtin_amdgcn_fence(__ATOMIC_RELEASE, "agent");
;       asm volatile("s_waitcnt vmcnt(0)" ::: "memory");
;       const unsigned og = xb_add(&bar[XB_TOP], 1u);
;       const unsigned tg = og / nx;
;       if (og + 1u == (tg + 1u) * nx) xb_add(&bar[XB_TOPGEN], 1u);
;       else XB_SPIN(xb_ld(&bar[XB_TOPGEN]) == tg, bar);
;       __builtin_amdgcn_fence(__ATOMIC_ACQUIRE, "agent");
;       xb_add(&bar[XB_XGEN(b.x)], 1u);
;       asm volatile("s_waitcnt vmcnt(0)" ::: "memory");
;     } else {
;       XB_SPIN(xb_ld(&bar[XB_XGEN(b.x)]) == gen, bar);
;       __builtin_amdgcn_fence(__ATOMIC_ACQUIRE, "agent");
;       asm volatile("s_waitcnt vmcnt(0)" ::: "memory");
;     }
;   }
;   __syncthreads();
; }
.LBB0_115:
	s_waitcnt vmcnt(0)
	s_barrier
	s_and_saveexec_b64 s[6:7], s[4:5]
	s_cbranch_execz .LBB0_167
	s_waitcnt vmcnt(0) lgkmcnt(0)
	s_add_u32 s98, s98, 1
	v_mov_b32_e32 v253, 0x12810
	ds_read_b32 v254, v253
	ds_read_b32 v253, v253 offset:4
	s_lshl_b32 s101, s33, 8
	s_add_u32 s99, s101, 5120
	s_waitcnt lgkmcnt(0)
	v_readfirstlane_b32 s100, v254
	v_mov_b32_e32 v254, s99
	v_readfirstlane_b32 s99, v253
	s_nop 0
	v_mov_b32_e32 v253, v254
	v_mov_b32_e32 v254, 1
	global_atomic_add v254, v253, v254, s[44:45] offset:64 sc0
	buffer_inv sc1
	s_mul_i32 s100, s100, s98
	s_mul_i32 s99, s99, s98
	s_waitcnt vmcnt(0)
	v_add_u32_e32 v254, 1, v254
	v_cmp_ne_u32_e32 vcc, s100, v254
	s_cbranch_vccnz .Lgb_wait_2
	buffer_wbl2 sc1
	s_waitcnt vmcnt(0)
	v_mov_b32_e32 v254, 1
	v_mov_b32_e32 v253, 9216
	global_atomic_add v253, v254, s[44:45] offset:64
	global_atomic_add v253, v254, s[44:45] offset:320
	global_atomic_add v253, v254, s[44:45] offset:576
	global_atomic_add v253, v254, s[44:45] offset:832
	global_atomic_add v253, v254, s[44:45] offset:1088
	global_atomic_add v253, v254, s[44:45] offset:1344
	global_atomic_add v253, v254, s[44:45] offset:1600
	global_atomic_add v253, v254, s[44:45] offset:1856
	v_mov_b32_e32 v253, 11264
	global_atomic_add v253, v254, s[44:45] offset:64
	global_atomic_add v253, v254, s[44:45] offset:320
	global_atomic_add v253, v254, s[44:45] offset:576
	global_atomic_add v253, v254, s[44:45] offset:832
	global_atomic_add v253, v254, s[44:45] offset:1088
	global_atomic_add v253, v254, s[44:45] offset:1344
	global_atomic_add v253, v254, s[44:45] offset:1600
	global_atomic_add v253, v254, s[44:45] offset:1856

; __device__ void phase_norm_mod(KParams& p, int bid, int nb, char* smem) {
;   const int lane = threadIdx.x & 63, w = threadIdx.x >> 6;
;   for (int t = bid * 4 + w; t < T + TC; t += nb * 4) {
;     const bool isx = t < T;
;     const float* src = isx ? (p.x + (size_t)t * D) : (p.ctx + (size_t)(t - T) * D);
;     const int mrow = isx ? (t / L) : 4;
;     float4 v[8];
;     float ss = 0.f;
; #pragma unroll
;     for (int c = 0; c < 8; ++c) {
;       v[c] = *reinterpret_cast<const float4*>(src + c * 256 + lane * 4);
;       ss += v[c].x * v[c].x + v[c].y * v[c].y + v[c].z * v[c].z + v[c].w * v[c].w;
;     }
;     ss = wave_sum_fast(ss);
;     const float rstd = rsqrtf(ss * (1.f / D) + EPS);
.Lgb_wd_2:
.LBB0_167:
	s_or_b64 exec, exec, s[6:7]
	v_lshrrev_b32_e32 v143, 6, v0
	v_lshl_or_b32 v186, s2, 2, v143
	s_movk_i32 s3, 0x2400
	s_mov_b64 s[8:9], s[0:1]
	v_cmp_gt_i32_e32 vcc, s3, v186
	v_ashrrev_i32_e32 v187, 31, v186
	v_lshlrev_b32_e32 v190, 2, v184
	v_mbcnt_lo_u32_b32 v191, -1, 0
	v_lshlrev_b32_e32 v188, 4, v184
	s_waitcnt lgkmcnt(0)
	s_barrier
	s_and_saveexec_b64 s[10:11], vcc
	s_cbranch_execz .LBB0_174
	s_load_dwordx2 s[22:23], s[8:9], 0x0
	s_load_dwordx2 s[24:25], s[8:9], 0x10
	s_load_dwordx2 s[16:17], s[8:9], 0x30
	s_load_dwordx2 s[18:19], s[8:9], 0xf8
	v_mov_b32_e32 v189, 0
	v_or_b32_e32 v8, 0x400, v190
	v_lshlrev_b32_e32 v10, 2, v8
	v_mov_b32_e32 v11, v189
	v_mbcnt_hi_u32_b32 v2, -1, v191
	s_waitcnt lgkmcnt(0)
	v_lshl_add_u64 v[56:57], s[16:17], 0, v[10:11]
	v_or_b32_e32 v10, 0x500, v190
	v_and_b32_e32 v4, 64, v2
	v_lshlrev_b32_e32 v12, 2, v10
	v_mov_b32_e32 v13, v189
	v_xor_b32_e32 v3, 16, v2
	v_add_u32_e32 v4, 64, v4
	v_lshl_add_u64 v[58:59], s[16:17], 0, v[12:13]
	v_or_b32_e32 v12, 0x600, v190
	v_cmp_lt_i32_e32 vcc, v3, v4
	v_lshlrev_b32_e32 v14, 2, v12
	v_mov_b32_e32 v15, v189
	v_cndmask_b32_e32 v3, v2, v3, vcc
	s_load_dwordx2 s[12:13], s[8:9], 0x188
	s_load_dwordx2 s[20:21], s[8:9], 0x108
	v_lshl_add_u64 v[60:61], s[16:17], 0, v[14:15]
	v_or_b32_e32 v14, 0x700, v190
	v_lshlrev_b32_e32 v90, 2, v3
	v_xor_b32_e32 v3, 32, v2
	v_lshlrev_b32_e32 v16, 2, v14
	v_mov_b32_e32 v17, v189
	v_cmp_lt_i32_e32 vcc, v3, v4
	v_lshl_add_u64 v[62:63], s[16:17], 0, v[16:17]
	v_lshlrev_b64 v[16:17], 11, v[186:187]
	v_cndmask_b32_e32 v2, v2, v3, vcc
	s_lshl_b32 s14, s34, 2
	v_or_b32_e32 v16, v16, v190
	v_lshlrev_b32_e32 v91, 2, v2
	v_or_b32_e32 v2, 0x100, v190
	v_or_b32_e32 v4, 0x200, v190
	v_or_b32_e32 v6, 0x300, v190
	s_ashr_i32 s15, s14, 31
	v_lshl_add_u64 v[16:17], s[18:19], 0, v[16:17]
	s_mov_b64 s[18:19], 0x400
	v_cmp_eq_u32_e64 s[6:7], 0, v184
	v_lshl_add_u64 v[54:55], s[16:17], 0, v[188:189]
	s_waitcnt lgkmcnt(0)
	v_lshl_add_u64 v[64:65], v[186:187], 2, s[20:21]
	s_lshl_b64 s[16:17], s[14:15], 2
	v_lshl_add_u64 v[66:67], v[16:17], 0, s[18:19]
	s_lshl_b64 s[18:19], s[14:15], 11
	s_mov_b64 s[20:21], 0
	s_movk_i32 s3, 0x2000
	v_mov_b32_e32 v92, s25
	v_mov_b32_e32 v93, s23
	v_mov_b32_e32 v94, s24
	v_mov_b32_e32 v95, s22
	v_lshlrev_b32_e32 v68, 2, v190
	v_mov_b32_e32 v69, v189
	s_movk_i32 s26, 0x1000
	v_mov_b32_e32 v96, 0x358637bd
	s_mov_b32 s27, 0x800000
	s_mov_b64 s[22:23], 0x2000
	v_lshlrev_b32_e32 v70, 2, v2
	v_mov_b32_e32 v71, v189
	v_lshlrev_b32_e32 v72, 2, v4
	v_mov_b32_e32 v73, v189
	v_lshlrev_b32_e32 v74, 2, v6
	v_mov_b32_e32 v75, v189
	v_lshlrev_b32_e32 v76, 2, v8
	v_mov_b32_e32 v77, v189
	v_lshlrev_b32_e32 v78, 2, v10
	v_mov_b32_e32 v79, v189
	v_lshlrev_b32_e32 v80, 2, v12
	v_mov_b32_e32 v81, v189
	v_lshlrev_b32_e32 v82, 2, v14
	v_mov_b32_e32 v83, v189
	s_mov_b32 s28, 0x42fe0000
	s_mov_b32 s29, 0x40c0c00
	s_movk_i32 s30, 0x23ff
	v_mov_b64_e32 v[84:85], v[186:187]
	s_branch .LBB0_170

; __device__ __forceinline__ unsigned xb_ld(unsigned* p)              { return __hip_atomic_load(p, __ATOMIC_RELAXED, __HIP_MEMORY_SCOPE_AGENT); }
; __device__ __forceinline__ unsigned xb_add(unsigned* p, unsigned v) { return __hip_atomic_fetch_add(p, v, __ATOMIC_RELAXED, __HIP_MEMORY_SCOPE_AGENT); }
; #define XB_SPIN(cond, bar) do { unsigned _sp = 0; while (cond) { __builtin_amdgcn_s_sleep(1); \
;     if ((++_sp & 255u) == 0u) { if (xb_ld(&(bar)[XB_TMO])) break; if (_sp > XB_SPIN_CAP) { atomicAdd(&(bar)[XB_TMO], 1u); break; } } } } while (0)
; __device__ __forceinline__ void xcd_barrier(const XcdBarrier& b) {
;   asm volatile("s_waitcnt vmcnt(0)" ::: "memory");
;   __syncthreads();
;   if (threadIdx.x == 0) {
;     unsigned* bar = b.bar;
;     __builtin_amdgcn_s_waitcnt(0);
;     unsigned nloc = b.st[0], nx = b.st[1];
;     if (nloc == 0u) { xcd_barrier_complete(bar, b.x, nloc, nx); b.st[0] = nloc; b.st[1] = nx; }
;     const unsigned old = xb_add(&bar[XB_XSUB(b.x)], 1u);
;     const unsigned gen = old / nloc;
;     if (old + 1u == (gen + 1u) * nloc) {
;       __builtin_amdgcn_fence(__ATOMIC_RELEASE, "agent");
;       asm volatile("s_waitcnt vmcnt(0)" ::: "memory");
;       const unsigned og = xb_add(&bar[XB_TOP], 1u);
;       const unsigned tg = og / nx;
;       if (og + 1u == (tg + 1u) * nx) xb_add(&bar[XB_TOPGEN], 1u);
;       else XB_SPIN(xb_ld(&bar[XB_TOPGEN]) == tg, bar);
;       __builtin_amdgcn_fence(__ATOMIC_ACQUIRE, "agent");
;       xb_add(&bar[XB_XGEN(b.x)], 1u);
;       asm volatile("s_waitcnt vmcnt(0)" ::: "memory");
;     } else {
;       XB_SPIN(xb_ld(&bar[XB_XGEN(b.x)]) == gen, bar);
;       __builtin_amdgcn_fence(__ATOMIC_ACQUIRE, "agent");
;       asm volatile("s_waitcnt vmcnt(0)" ::: "memory");
;     }
;   }
;   __syncthreads();
; }
.LBB0_179:
	s_or_b64 exec, exec, s[10:11]
	s_waitcnt vmcnt(0)
	s_barrier
	s_and_saveexec_b64 s[6:7], s[4:5]
	s_cbranch_execz .LBB0_231
	s_waitcnt vmcnt(0) lgkmcnt(0)
	s_add_u32 s98, s98, 1
	v_mov_b32_e32 v253, 0x12810
	ds_read_b32 v254, v253
	ds_read_b32 v253, v253 offset:4
	s_lshl_b32 s101, s33, 8
	s_add_u32 s99, s101, 5120
	s_waitcnt lgkmcnt(0)
	v_readfirstlane_b32 s100, v254
	v_mov_b32_e32 v254, s99
	v_readfirstlane_b32 s99, v253
	s_nop 0
	v_mov_b32_e32 v253, v254
	v_mov_b32_e32 v254, 1
	global_atomic_add v254, v253, v254, s[44:45] offset:64 sc0
	buffer_inv sc1
	s_mul_i32 s100, s100, s98
	s_mul_i32 s99, s99, s98
	s_waitcnt vmcnt(0)
	v_add_u32_e32 v254, 1, v254
	v_cmp_ne_u32_e32 vcc, s100, v254
	s_cbranch_vccnz .Lgb_wait_3
	buffer_wbl2 sc1
	s_waitcnt vmcnt(0)
	v_mov_b32_e32 v254, 1
	v_mov_b32_e32 v253, 9216
	global_atomic_add v253, v254, s[44:45] offset:64
	global_atomic_add v253, v254, s[44:45] offset:320
	global_atomic_add v253, v254, s[44:45] offset:576
	global_atomic_add v253, v254, s[44:45] offset:832
	global_atomic_add v253, v254, s[44:45] offset:1088
	global_atomic_add v253, v254, s[44:45] offset:1344
	global_atomic_add v253, v254, s[44:45] offset:1600
	global_atomic_add v253, v254, s[44:45] offset:1856
	v_mov_b32_e32 v253, 11264
	global_atomic_add v253, v254, s[44:45] offset:64
	global_atomic_add v253, v254, s[44:45] offset:320
	global_atomic_add v253, v254, s[44:45] offset:576
	global_atomic_add v253, v254, s[44:45] offset:832
	global_atomic_add v253, v254, s[44:45] offset:1088
	global_atomic_add v253, v254, s[44:45] offset:1344
	global_atomic_add v253, v254, s[44:45] offset:1600
	global_atomic_add v253, v254, s[44:45] offset:1856

; __device__ void phase_inproj(KParams& p, int bid, int nb, char* smem) {
;   const bool aware = (nb & 7) == 0;
;   const int start = aware ? (bid >> 3) : bid, step = aware ? (nb >> 3) : nb, end = aware ? (128 + 53) : 8 * (128 + 53);
;   const bf16_t* a8 = reinterpret_cast<const bf16_t*>(p.hx8a);
;   const bf16_t* b8 = reinterpret_cast<const bf16_t*>(p.w8);
;   for (int it = start; it < end; it += step) {
;     const int x = aware ? (bid & 7) : it / (128 + 53), s_ = aware ? it : it % (128 + 53);
;     if (s_ < 128) {
;       const int tn2 = s_ >> 3, m0_ = (8 * x + (s_ & 7)) * 128;
;       if (tn2 < 8) { EpiInAB epi{p.ABt, L}; gemm_tile_n256<true>(a8, D / 2, b8, D / 2, D / 2, m0_, tn2 * 256, epi, smem, p.ascale, p.wscale); }
.Lgb_wd_3:
.LBB0_231:
	s_or_b64 exec, exec, s[6:7]
	s_and_b32 s3, s34, 7
	s_ashr_i32 s10, s2, 3
	s_ashr_i32 s11, s34, 3
	s_cmp_eq_u32 s3, 0
	s_cselect_b64 s[48:49], -1, 0
	s_and_b64 s[8:9], s[48:49], exec
	s_movk_i32 s8, 0xb5
	s_cselect_b32 s3, s10, s2
	s_cselect_b32 s80, s8, 0x5a8
	s_mov_b64 s[6:7], s[0:1]
	s_cselect_b32 s35, s11, s34
	s_cmp_ge_i32 s3, s80
	v_lshlrev_b32_e32 v183, 1, v0
	v_and_b32_e32 v185, 15, v0
	s_waitcnt lgkmcnt(0)
	s_barrier
	s_cbranch_scc1 .LBB0_572
	s_load_dwordx8 s[20:27], s[6:7], 0xf8
	s_and_b32 s81, s2, 7
	s_load_dwordx4 s[28:31], s[6:7], 0x1c0
	s_load_dwordx8 s[36:43], s[6:7], 0x1a0
	v_writelane_b32 v252, s96, 2
	v_and_b32_e32 v2, 64, v135
	s_waitcnt lgkmcnt(0)
	s_add_u32 s18, s20, 0x1000000
	s_addc_u32 s19, s21, 0
	s_add_u32 s52, s24, 0x8000
	s_movk_i32 s82, 0x80
	v_writelane_b32 v252, s97, 3
	s_addc_u32 s53, s25, 0
	v_and_or_b32 v145, v1, 12, v2
	v_and_b32_e32 v164, 0x4f, v0
	v_and_or_b32 v165, v183, s82, v185
	s_movk_i32 s83, 0xc00
	v_mov_b32_e32 v137, 0
	s_mov_b64 s[54:55], 0x10000
	s_mov_b64 s[56:57], 0x20000
	s_mov_b64 s[58:59], 0x30000
	s_mov_b32 s84, 0x1ffffc0
	s_mov_b64 s[60:61], 0x80
	s_mov_b64 s[62:63], 0x10080
	s_mov_b64 s[64:65], 0x20080
	s_mov_b64 s[66:67], 0x30080
	s_movk_i32 s85, 0x1220
	s_movk_i32 s86, 0xf000
	s_movk_i32 s87, 0xfc00
	s_movk_i32 s88, 0xbef
	s_movk_i32 s89, 0x11ef
	s_movk_i32 s90, 0x1210
	s_movk_i32 s92, 0xbdf
	s_movk_i32 s93, 0x11df
	s_movk_i32 s95, 0xbcf
	s_movk_i32 s96, 0x11cf
	s_movk_i32 s97, 0x11f0
	s_movk_i32 s50, 0x3ff
	s_mov_b64 s[68:69], 0x40000
	s_mov_b64 s[70:71], 0x50000
	s_mov_b64 s[72:73], 0x60000
	s_mov_b64 s[74:75], 0x70000
	v_mov_b32_e32 v166, 0x38f
	v_mov_b32_e32 v167, 0x50
	v_mov_b32_e32 v168, 0x60
	v_mov_b32_e32 v169, 0x70
	s_mov_b32 s51, s3
	s_branch .LBB0_234

; __device__ __forceinline__ unsigned xb_ld(unsigned* p)              { return __hip_atomic_load(p, __ATOMIC_RELAXED, __HIP_MEMORY_SCOPE_AGENT); }
; __device__ __forceinline__ unsigned xb_add(unsigned* p, unsigned v) { return __hip_atomic_fetch_add(p, v, __ATOMIC_RELAXED, __HIP_MEMORY_SCOPE_AGENT); }
; #define XB_SPIN(cond, bar) do { unsigned _sp = 0; while (cond) { __builtin_amdgcn_s_sleep(1); \
;     if ((++_sp & 255u) == 0u) { if (xb_ld(&(bar)[XB_TMO])) break; if (_sp > XB_SPIN_CAP) { atomicAdd(&(bar)[XB_TMO], 1u); break; } } } } while (0)
; __device__ __forceinline__ void xcd_barrier(const XcdBarrier& b) {
;   asm volatile("s_waitcnt vmcnt(0)" ::: "memory");
;   __syncthreads();
;   if (threadIdx.x == 0) {
;     unsigned* bar = b.bar;
;     __builtin_amdgcn_s_waitcnt(0);
;     unsigned nloc = b.st[0], nx = b.st[1];
;     if (nloc == 0u) { xcd_barrier_complete(bar, b.x, nloc, nx); b.st[0] = nloc; b.st[1] = nx; }
;     const unsigned old = xb_add(&bar[XB_XSUB(b.x)], 1u);
;     const unsigned gen = old / nloc;
;     if (old + 1u == (gen + 1u) * nloc) {
;       __builtin_amdgcn_fence(__ATOMIC_RELEASE, "agent");
;       asm volatile("s_waitcnt vmcnt(0)" ::: "memory");
;       const unsigned og = xb_add(&bar[XB_TOP], 1u);
;       const unsigned tg = og / nx;
;       if (og + 1u == (tg + 1u) * nx) xb_add(&bar[XB_TOPGEN], 1u);
;       else XB_SPIN(xb_ld(&bar[XB_TOPGEN]) == tg, bar);
;       __builtin_amdgcn_fence(__ATOMIC_ACQUIRE, "agent");
;       xb_add(&bar[XB_XGEN(b.x)], 1u);
;       asm volatile("s_waitcnt vmcnt(0)" ::: "memory");
;     } else {
;       XB_SPIN(xb_ld(&bar[XB_XGEN(b.x)]) == gen, bar);
;       __builtin_amdgcn_fence(__ATOMIC_ACQUIRE, "agent");
;       asm volatile("s_waitcnt vmcnt(0)" ::: "memory");
;     }
;   }
;   __syncthreads();
; }
.LBB0_572:
	s_waitcnt vmcnt(0)
	s_waitcnt lgkmcnt(0)
	s_barrier
	s_and_saveexec_b64 s[6:7], s[4:5]
	s_cbranch_execz .LBB0_624
	s_waitcnt vmcnt(0) lgkmcnt(0)
	s_add_u32 s98, s98, 1
	v_mov_b32_e32 v253, 0x12810
	ds_read_b32 v254, v253
	ds_read_b32 v253, v253 offset:4
	s_lshl_b32 s101, s33, 8
	s_add_u32 s99, s101, 5120
	s_waitcnt lgkmcnt(0)
	v_readfirstlane_b32 s100, v254
	v_mov_b32_e32 v254, s99
	v_readfirstlane_b32 s99, v253
	s_nop 0
	v_mov_b32_e32 v253, v254
	v_mov_b32_e32 v254, 1
	global_atomic_add v254, v253, v254, s[44:45] offset:64 sc0
	buffer_inv sc1
	s_mul_i32 s100, s100, s98
	s_mul_i32 s99, s99, s98
	s_waitcnt vmcnt(0)
	v_add_u32_e32 v254, 1, v254
	v_cmp_ne_u32_e32 vcc, s100, v254
	s_cbranch_vccnz .Lgb_wait_4
	buffer_wbl2 sc1
	s_waitcnt vmcnt(0)
	v_mov_b32_e32 v254, 1
	v_mov_b32_e32 v253, 9216
	global_atomic_add v253, v254, s[44:45] offset:64
	global_atomic_add v253, v254, s[44:45] offset:320
	global_atomic_add v253, v254, s[44:45] offset:576
	global_atomic_add v253, v254, s[44:45] offset:832
	global_atomic_add v253, v254, s[44:45] offset:1088
	global_atomic_add v253, v254, s[44:45] offset:1344
	global_atomic_add v253, v254, s[44:45] offset:1600
	global_atomic_add v253, v254, s[44:45] offset:1856
	v_mov_b32_e32 v253, 11264
	global_atomic_add v253, v254, s[44:45] offset:64
	global_atomic_add v253, v254, s[44:45] offset:320
	global_atomic_add v253, v254, s[44:45] offset:576
	global_atomic_add v253, v254, s[44:45] offset:832
	global_atomic_add v253, v254, s[44:45] offset:1088
	global_atomic_add v253, v254, s[44:45] offset:1344
	global_atomic_add v253, v254, s[44:45] offset:1600
	global_atomic_add v253, v254, s[44:45] offset:1856

; __device__ void dft_fold_rows(KParams& p, int bid, int nb, char* smem) {
;   const int lane = threadIdx.x & 63, w = threadIdx.x >> 6;
;   bf16_t* sr = reinterpret_cast<bf16_t*>(smem + w * 8192);
;   for (int row = bid * 4 + w; row < NB * 1024; row += nb * 4) {
;     const bf16_t* A = p.ABt + (size_t)row * 4096;
;     bf16_t* F = p.Fs + (size_t)row * 2048;
;     __builtin_amdgcn_wave_barrier();
;     {
;       const uint4 q0 = *reinterpret_cast<const uint4*>(A + (0 * 64 + lane) * 8), q1 = *reinterpret_cast<const uint4*>(A + (1 * 64 + lane) * 8);
.Lgb_wd_4:
.LBB0_624:
	s_or_b64 exec, exec, s[6:7]
	s_movk_i32 s6, 0x1000
	s_mov_b64 s[14:15], s[0:1]
	v_cmp_gt_i32_e32 vcc, s6, v186
	s_waitcnt lgkmcnt(0)
	s_barrier
	s_and_saveexec_b64 s[10:11], vcc
	s_cbranch_execz .LBB0_633
	v_mbcnt_hi_u32_b32 v2, -1, v191
	v_and_b32_e32 v4, 64, v2
	v_xor_b32_e32 v3, 16, v2
	v_add_u32_e32 v4, 64, v4
	v_cmp_lt_i32_e32 vcc, v3, v4
	s_load_dwordx2 s[20:21], s[14:15], 0x178
	s_load_dwordx2 s[18:19], s[14:15], 0x1a0
	s_load_dwordx2 s[12:13], s[14:15], 0x228
	v_cndmask_b32_e32 v3, v2, v3, vcc
	v_lshlrev_b32_e32 v42, 2, v3
	v_xor_b32_e32 v3, 32, v2
	v_cmp_lt_i32_e32 vcc, v3, v4
	v_lshlrev_b32_e32 v40, 13, v143
	s_lshl_b32 s16, s34, 2
	v_cndmask_b32_e32 v2, v2, v3, vcc
	v_lshlrev_b32_e32 v43, 2, v2
	v_lshlrev_b32_e32 v2, 5, v184
	v_sub_u32_e32 v44, v40, v2
	v_lshlrev_b64 v[2:3], 13, v[186:187]
	v_or_b32_e32 v2, v2, v188
	s_waitcnt lgkmcnt(0)
	v_lshl_add_u64 v[2:3], s[18:19], 0, v[2:3]
	s_mov_b64 s[18:19], 0x1c00
	v_lshl_add_u64 v[34:35], v[2:3], 0, s[18:19]
	v_lshlrev_b64 v[2:3], 12, v[186:187]
	v_or_b32_e32 v41, v40, v188
	s_ashr_i32 s17, s16, 31
	v_lshl_or_b32 v2, v184, 5, v2
	v_cmp_eq_u32_e64 s[6:7], 0, v184
	v_cmp_ne_u32_e64 s[8:9], 0, v184
	s_lshl_b64 s[18:19], s[16:17], 13
	v_lshl_add_u64 v[36:37], s[20:21], 0, v[2:3]
	s_lshl_b64 s[20:21], s[16:17], 12
	s_mov_b64 s[22:23], 0
	v_add_u32_e32 v45, v41, v188
	v_mov_b32_e32 v39, 0
	s_movk_i32 s17, 0xfff
	v_mov_b32_e32 v46, v186
	s_branch .LBB0_627

; __device__ __forceinline__ unsigned xb_ld(unsigned* p)              { return __hip_atomic_load(p, __ATOMIC_RELAXED, __HIP_MEMORY_SCOPE_AGENT); }
; __device__ __forceinline__ unsigned xb_add(unsigned* p, unsigned v) { return __hip_atomic_fetch_add(p, v, __ATOMIC_RELAXED, __HIP_MEMORY_SCOPE_AGENT); }
; #define XB_SPIN(cond, bar) do { unsigned _sp = 0; while (cond) { __builtin_amdgcn_s_sleep(1); \
;     if ((++_sp & 255u) == 0u) { if (xb_ld(&(bar)[XB_TMO])) break; if (_sp > XB_SPIN_CAP) { atomicAdd(&(bar)[XB_TMO], 1u); break; } } } } while (0)
; __device__ __forceinline__ void xcd_barrier(const XcdBarrier& b) {
;   asm volatile("s_waitcnt vmcnt(0)" ::: "memory");
;   __syncthreads();
;   if (threadIdx.x == 0) {
;     unsigned* bar = b.bar;
;     __builtin_amdgcn_s_waitcnt(0);
;     unsigned nloc = b.st[0], nx = b.st[1];
;     if (nloc == 0u) { xcd_barrier_complete(bar, b.x, nloc, nx); b.st[0] = nloc; b.st[1] = nx; }
;     const unsigned old = xb_add(&bar[XB_XSUB(b.x)], 1u);
;     const unsigned gen = old / nloc;
;     if (old + 1u == (gen + 1u) * nloc) {
;       __builtin_amdgcn_fence(__ATOMIC_RELEASE, "agent");
;       asm volatile("s_waitcnt vmcnt(0)" ::: "memory");
;       const unsigned og = xb_add(&bar[XB_TOP], 1u);
;       const unsigned tg = og / nx;
;       if (og + 1u == (tg + 1u) * nx) xb_add(&bar[XB_TOPGEN], 1u);
;       else XB_SPIN(xb_ld(&bar[XB_TOPGEN]) == tg, bar);
;       __builtin_amdgcn_fence(__ATOMIC_ACQUIRE, "agent");
;       xb_add(&bar[XB_XGEN(b.x)], 1u);
;       asm volatile("s_waitcnt vmcnt(0)" ::: "memory");
;     } else {
;       XB_SPIN(xb_ld(&bar[XB_XGEN(b.x)]) == gen, bar);
;       __builtin_amdgcn_fence(__ATOMIC_ACQUIRE, "agent");
;       asm volatile("s_waitcnt vmcnt(0)" ::: "memory");
;     }
;   }
;   __syncthreads();
; }
.LBB0_677:
	s_or_b64 exec, exec, s[12:13]
	s_waitcnt vmcnt(0)
	s_waitcnt lgkmcnt(0)
	s_barrier
	s_and_saveexec_b64 s[6:7], s[4:5]
	s_cbranch_execz .LBB0_729
	s_waitcnt vmcnt(0) lgkmcnt(0)
	s_add_u32 s98, s98, 1
	v_mov_b32_e32 v253, 0x12810
	ds_read_b32 v254, v253
	ds_read_b32 v253, v253 offset:4
	s_lshl_b32 s101, s33, 8
	s_add_u32 s99, s101, 5120
	s_waitcnt lgkmcnt(0)
	v_readfirstlane_b32 s100, v254
	v_mov_b32_e32 v254, s99
	v_readfirstlane_b32 s99, v253
	s_nop 0
	v_mov_b32_e32 v253, v254
	v_mov_b32_e32 v254, 1
	global_atomic_add v254, v253, v254, s[44:45] offset:64 sc0
	buffer_inv sc1
	s_mul_i32 s100, s100, s98
	s_mul_i32 s99, s99, s98
	s_waitcnt vmcnt(0)
	v_add_u32_e32 v254, 1, v254
	v_cmp_ne_u32_e32 vcc, s100, v254
	s_cbranch_vccnz .Lgb_wait_5
	buffer_wbl2 sc1
	s_waitcnt vmcnt(0)
	v_mov_b32_e32 v254, 1
	v_mov_b32_e32 v253, 9216
	global_atomic_add v253, v254, s[44:45] offset:64
	global_atomic_add v253, v254, s[44:45] offset:320
	global_atomic_add v253, v254, s[44:45] offset:576
	global_atomic_add v253, v254, s[44:45] offset:832
	global_atomic_add v253, v254, s[44:45] offset:1088
	global_atomic_add v253, v254, s[44:45] offset:1344
	global_atomic_add v253, v254, s[44:45] offset:1600
	global_atomic_add v253, v254, s[44:45] offset:1856
	v_mov_b32_e32 v253, 11264
	global_atomic_add v253, v254, s[44:45] offset:64
	global_atomic_add v253, v254, s[44:45] offset:320
	global_atomic_add v253, v254, s[44:45] offset:576
	global_atomic_add v253, v254, s[44:45] offset:832
	global_atomic_add v253, v254, s[44:45] offset:1088
	global_atomic_add v253, v254, s[44:45] offset:1344
	global_atomic_add v253, v254, s[44:45] offset:1600
	global_atomic_add v253, v254, s[44:45] offset:1856

; __device__ __forceinline__ int opaque_tid() { int t = threadIdx.x; asm volatile("" : "+v"(t)); return t; }
; __device__ void ssd_task(KParams& p, int task, char* smem) {
;   const int dir = task & 1, ph = (task >> 1) & 1, h = (task >> 2) & 15, b = task >> 6;
;   const int tid = opaque_tid(), lane = tid & 63, w = tid >> 6;
;   const int g = h >> 3, lr0 = lane & 15, lq0 = lane >> 4;
;   const float a = -__expf(dir ? p.a_log_b[h] : p.a_log_f[h]);
;   char* sCc = smem; char* sBc = smem + 16384; char* sBT = smem + 32768; char* sXT = smem + 49152; char* sHb = smem + 57344;
;   float* se = reinterpret_cast<float*>(smem + 73728);
;   float* sdt = se + 64; float* sw = se + 128; float* sy = se + 192; float* stot = se + 256;
;   bf16_t* yo = reinterpret_cast<bf16_t*>(dir ? p.yb : p.yf);
;   f32x4 H[2][2];
; #pragma unroll
;   for (int i = 0; i < 2; ++i)
; #pragma unroll
;     for (int j = 0; j < 2; ++j) H[i][j] = f32x4{0.f, 0.f, 0.f, 0.f};
;   __syncthreads();
;   for (int i = tid; i < 512; i += NTHREADS) reinterpret_cast<uint4*>(sHb)[i] = uint4{0, 0, 0, 0};
;   const int crow = tid >> 4, cch = tid & 15;
;   const int trow = tid >> 3, tch = tid & 7;
;   uint4 rC0, rC1, rC2, rC3, rB0, rB1, rB2, rB3, rT0, rT1, rT2, rT3, rX;
;   rC0 = rC1 = rC2 = rC3 = rB0 = rB1 = rB2 = rB3 = uint4{0, 0, 0, 0};
;   float rdt = 0.f;
.Lgb_wd_5:
.LBB0_729:
	s_or_b64 exec, exec, s[6:7]
	v_readlane_b32 s6, v252, 0
	v_readlane_b32 s7, v252, 1
	s_mov_b64 s[26:27], s[0:1]
	s_andn2_b64 vcc, exec, s[6:7]
	s_waitcnt lgkmcnt(0)
	s_barrier
	s_cbranch_vccnz .LBB0_760
	s_load_dwordx4 s[20:23], s[26:27], 0x80
	s_load_dwordx2 s[24:25], s[26:27], 0x200
	s_load_dwordx8 s[12:19], s[26:27], 0x1e0
	s_add_u32 s46, s26, 0x1e8
	s_addc_u32 s47, s27, 0
	s_add_u32 s62, s26, 0x1e0
	v_mov_b32_e32 v99, 0
	s_addc_u32 s63, s27, 0
	s_mov_b32 s29, 0
	s_movk_i32 s64, 0x208
	s_movk_i32 s65, 0x200
	s_movk_i32 s66, 0xff
	s_movk_i32 s67, 0x4000
	s_mov_b32 s68, 0x8000
	s_mov_b32 s69, 0xc000
	s_movk_i32 s70, 0xf0
	s_movk_i32 s71, 0x70
	s_movk_i32 s72, 0x1d0
	v_mov_b32_e32 v120, 0x12400
	s_movk_i32 s73, 0xc00
	s_mov_b32 s74, 0x20000
	v_mov_b32_e32 v121, 0xe000
	v_mov_b32_e32 v150, v99
	v_mov_b32_e32 v151, v99
	v_mov_b32_e32 v152, v99
	v_mov_b32_e32 v153, v99
	v_mov_b32_e32 v122, 0x12200
	s_mov_b32 s75, s2
	s_branch .LBB0_732

; __device__ __forceinline__ float bflo(uint32_t w) { return __uint_as_float(w << 16); }
; __device__ __forceinline__ float bfhi(uint32_t w) { return __uint_as_float(w & 0xffff0000u); }
; __device__ void phase_ssm_post(KParams& p, int bid, int nb, char* smem) {
;   const int lane = threadIdx.x & 63, w = threadIdx.x >> 6;
;   for (int t = bid * 4 + w; t < T; t += nb * 4) {
;     float y[4][4];
;     float ss0 = 0.f, ss1 = 0.f;
; #pragma unroll
;     for (int c = 0; c < 4; ++c) {
;       const int c0 = c * 256 + lane * 4;
;       const int h = c0 >> 6;
;       const float dsk = p.d_skip_f[h] + p.d_skip_b[h];
;       const uint2 aq = *reinterpret_cast<const uint2*>(reinterpret_cast<const bf16_t*>(p.yf) + (size_t)t * 1024 + c0);
;       const uint2 bb = *reinterpret_cast<const uint2*>(reinterpret_cast<const bf16_t*>(p.yb) + (size_t)t * 1024 + c0);
;       const float4 a = float4{bflo(aq.x), bfhi(aq.x), bflo(aq.y), bfhi(aq.y)};
;       const float4 bq = float4{bflo(bb.x), bfhi(bb.x), bflo(bb.y), bfhi(bb.y)};
;       const uint2 xq = *reinterpret_cast<const uint2*>(p.act_tm + (size_t)t * DXBC + c0);
;       const uint2 zz = *reinterpret_cast<const uint2*>(p.z + (size_t)t * 1024 + c0);
.Lgb_wd_6:
.LBB0_1000:
	s_or_b64 exec, exec, s[6:7]
	s_movk_i32 s6, 0x2000
	v_mov_b32_e32 v191, 0
	s_mov_b64 s[16:17], s[0:1]
	v_cmp_gt_i32_e64 s[6:7], s6, v186
	v_lshlrev_b32_e32 v134, 2, v190
	s_waitcnt lgkmcnt(0)
	s_barrier
	s_and_saveexec_b64 s[18:19], s[6:7]
	s_cbranch_execz .LBB0_1005
	v_cmp_lt_i32_e32 vcc, v179, v180
	s_load_dwordx4 s[12:15], s[16:17], 0x90
	s_load_dwordx2 s[22:23], s[16:17], 0xa0
	v_cndmask_b32_e32 v2, v178, v179, vcc
	v_cmp_lt_i32_e32 vcc, v181, v180
	s_load_dwordx4 s[24:27], s[16:17], 0x208
	s_load_dwordx2 s[28:29], s[16:17], 0x228
	s_load_dwordx2 s[30:31], s[16:17], 0x1f0
	s_load_dwordx2 s[36:37], s[16:17], 0x1a8
	s_load_dwordx2 s[38:39], s[16:17], 0x118
	s_load_dwordx2 s[40:41], s[16:17], 0x128
	v_lshlrev_b32_e32 v39, 2, v2
	v_cndmask_b32_e32 v2, v178, v181, vcc
	v_or_b32_e32 v6, 0x100, v190
	v_or_b32_e32 v10, 0x200, v190
	v_or_b32_e32 v14, 0x300, v190
	v_lshlrev_b32_e32 v74, 2, v2
	v_lshrrev_b32_e32 v2, 2, v184
	v_lshrrev_b32_e32 v6, 4, v6
	v_lshrrev_b32_e32 v10, 4, v10
	v_lshrrev_b32_e32 v14, 4, v14
	s_lshl_b32 s20, s34, 2
	v_and_b32_e32 v4, 12, v2
	v_mov_b32_e32 v5, v191
	v_and_b32_e32 v8, 28, v6
	v_mov_b32_e32 v9, v191
	v_and_b32_e32 v12, 44, v10
	v_mov_b32_e32 v13, v191
	v_and_b32_e32 v16, 60, v14
	v_mov_b32_e32 v17, v191
	s_waitcnt lgkmcnt(0)
	v_lshl_add_u64 v[2:3], s[12:13], 0, v[4:5]
	v_lshl_add_u64 v[6:7], s[12:13], 0, v[8:9]
	v_lshl_add_u64 v[10:11], s[12:13], 0, v[12:13]
	v_lshl_add_u64 v[14:15], s[12:13], 0, v[16:17]
	v_mov_b32_e32 v135, v191
	v_lshlrev_b32_e32 v24, 1, v190
	v_mov_b32_e32 v25, v191
	s_ashr_i32 s21, s20, 31
	v_lshlrev_b64 v[34:35], 12, v[186:187]
	s_movk_i32 s12, 0xc00
	v_mov_b64_e32 v[36:37], s[30:31]
	v_lshl_add_u64 v[4:5], s[14:15], 0, v[4:5]
	v_lshl_add_u64 v[8:9], s[14:15], 0, v[8:9]
	v_lshl_add_u64 v[12:13], s[14:15], 0, v[12:13]
	v_lshl_add_u64 v[16:17], s[14:15], 0, v[16:17]
	v_lshl_add_u64 v[18:19], s[22:23], 0, v[134:135]
	v_lshl_add_u64 v[20:21], s[24:25], 0, v[24:25]
	v_lshl_add_u64 v[22:23], s[26:27], 0, v[24:25]
	v_lshl_add_u64 v[24:25], s[36:37], 0, v[24:25]
	v_lshl_add_u64 v[26:27], s[38:39], 0, v[190:191]
	v_lshl_add_u64 v[28:29], v[186:187], 2, s[40:41]
	s_lshl_b64 s[14:15], s[20:21], 2
	v_lshlrev_b64 v[30:31], 11, v[186:187]
	s_lshl_b64 s[22:23], s[20:21], 11
	v_lshlrev_b32_e32 v32, 3, v184
	v_mov_b32_e32 v33, v191
	v_lshl_add_u64 v[34:35], s[28:29], 0, v[34:35]
	s_lshl_b64 s[24:25], s[20:21], 12
	v_mad_i64_i32 v[36:37], s[12:13], v186, s12, v[36:37]
	s_mul_i32 s26, s34, 0x3000
	s_mul_hi_i32 s27, s20, 0xc00
	s_mov_b64 s[28:29], 0
	s_mov_b32 s30, 0x3b000000
	v_mov_b32_e32 v38, 0x358637bd
	s_mov_b32 s21, 0x800000
	s_mov_b32 s31, 0x42fe0000
	s_mov_b32 s36, 0xc0c0500
	s_mov_b32 s37, 0x40c0c00
	s_movk_i32 s38, 0x1fff
	v_mov_b32_e32 v75, v186
	s_branch .LBB0_1003

; __device__ __forceinline__ unsigned xb_ld(unsigned* p)              { return __hip_atomic_load(p, __ATOMIC_RELAXED, __HIP_MEMORY_SCOPE_AGENT); }
; __device__ __forceinline__ unsigned xb_add(unsigned* p, unsigned v) { return __hip_atomic_fetch_add(p, v, __ATOMIC_RELAXED, __HIP_MEMORY_SCOPE_AGENT); }
; #define XB_SPIN(cond, bar) do { unsigned _sp = 0; while (cond) { __builtin_amdgcn_s_sleep(1); \
;     if ((++_sp & 255u) == 0u) { if (xb_ld(&(bar)[XB_TMO])) break; if (_sp > XB_SPIN_CAP) { atomicAdd(&(bar)[XB_TMO], 1u); break; } } } } while (0)
; __device__ __forceinline__ void xcd_barrier(const XcdBarrier& b) {
;   asm volatile("s_waitcnt vmcnt(0)" ::: "memory");
;   __syncthreads();
;   if (threadIdx.x == 0) {
;     unsigned* bar = b.bar;
;     __builtin_amdgcn_s_waitcnt(0);
;     unsigned nloc = b.st[0], nx = b.st[1];
;     if (nloc == 0u) { xcd_barrier_complete(bar, b.x, nloc, nx); b.st[0] = nloc; b.st[1] = nx; }
;     const unsigned old = xb_add(&bar[XB_XSUB(b.x)], 1u);
;     const unsigned gen = old / nloc;
;     if (old + 1u == (gen + 1u) * nloc) {
;       __builtin_amdgcn_fence(__ATOMIC_RELEASE, "agent");
;       asm volatile("s_waitcnt vmcnt(0)" ::: "memory");
;       const unsigned og = xb_add(&bar[XB_TOP], 1u);
;       const unsigned tg = og / nx;
;       if (og + 1u == (tg + 1u) * nx) xb_add(&bar[XB_TOPGEN], 1u);
;       else XB_SPIN(xb_ld(&bar[XB_TOPGEN]) == tg, bar);
;       __builtin_amdgcn_fence(__ATOMIC_ACQUIRE, "agent");
;       xb_add(&bar[XB_XGEN(b.x)], 1u);
;       asm volatile("s_waitcnt vmcnt(0)" ::: "memory");
;     } else {
;       XB_SPIN(xb_ld(&bar[XB_XGEN(b.x)]) == gen, bar);
;       __builtin_amdgcn_fence(__ATOMIC_ACQUIRE, "agent");
;       asm volatile("s_waitcnt vmcnt(0)" ::: "memory");
;     }
;   }
;   __syncthreads();
; }
.LBB0_1015:
	s_or_b64 exec, exec, s[12:13]
	s_waitcnt vmcnt(0)
	s_barrier
	s_and_saveexec_b64 s[12:13], s[4:5]
	s_cbranch_execz .LBB0_1067
	s_waitcnt vmcnt(0) lgkmcnt(0)
	s_add_u32 s98, s98, 1
	v_mov_b32_e32 v253, 0x12810
	ds_read_b32 v254, v253
	ds_read_b32 v253, v253 offset:4
	s_lshl_b32 s101, s33, 8
	s_add_u32 s99, s101, 5120
	s_waitcnt lgkmcnt(0)
	v_readfirstlane_b32 s100, v254
	v_mov_b32_e32 v254, s99
	v_readfirstlane_b32 s99, v253
	s_nop 0
	v_mov_b32_e32 v253, v254
	v_mov_b32_e32 v254, 1
	global_atomic_add v254, v253, v254, s[44:45] offset:64 sc0
	buffer_inv sc1
	s_mul_i32 s100, s100, s98
	s_mul_i32 s99, s99, s98
	s_waitcnt vmcnt(0)
	v_add_u32_e32 v254, 1, v254
	v_cmp_ne_u32_e32 vcc, s100, v254
	s_cbranch_vccnz .Lgb_wait_7
	buffer_wbl2 sc1
	s_waitcnt vmcnt(0)
	v_mov_b32_e32 v254, 1
	v_mov_b32_e32 v253, 9216
	global_atomic_add v253, v254, s[44:45] offset:64
	global_atomic_add v253, v254, s[44:45] offset:320
	global_atomic_add v253, v254, s[44:45] offset:576
	global_atomic_add v253, v254, s[44:45] offset:832
	global_atomic_add v253, v254, s[44:45] offset:1088
	global_atomic_add v253, v254, s[44:45] offset:1344
	global_atomic_add v253, v254, s[44:45] offset:1600
	global_atomic_add v253, v254, s[44:45] offset:1856
	v_mov_b32_e32 v253, 11264
	global_atomic_add v253, v254, s[44:45] offset:64
	global_atomic_add v253, v254, s[44:45] offset:320
	global_atomic_add v253, v254, s[44:45] offset:576
	global_atomic_add v253, v254, s[44:45] offset:832
	global_atomic_add v253, v254, s[44:45] offset:1088
	global_atomic_add v253, v254, s[44:45] offset:1344
	global_atomic_add v253, v254, s[44:45] offset:1600
	global_atomic_add v253, v254, s[44:45] offset:1856

; __device__ void phase_outproj(KParams& p, int bid, int nb, char* smem) {
;   const bool aware = (nb & 7) == 0;
;   const int start = aware ? (bid >> 3) : bid, step = aware ? (nb >> 3) : nb, end = aware ? 64 : 512;
;   const bf16_t* a8 = reinterpret_cast<const bf16_t*>(p.ycat8);
;   const bf16_t* b8 = reinterpret_cast<const bf16_t*>(p.wo8);
;   for (int it = start; it < end; it += step) {
;     const int x = aware ? (bid & 7) : (it >> 6), s_ = aware ? it : (it & 63);
;     EpiBf16 epi{reinterpret_cast<bf16_t*>(p.y_x), D};
;     gemm_tile_n256<true>(a8, D / 2, b8, D / 2, D / 2, (8 * x + (s_ & 7)) * 128, (s_ >> 3) * 256, epi, smem, p.yscale, p.woscale);
.Lgb_wd_7:
.LBB0_1067:
	s_or_b64 exec, exec, s[12:13]
	s_and_b64 s[12:13], s[48:49], exec
	s_cselect_b32 s42, 64, 0x200
	s_mov_b64 s[20:21], s[0:1]
	s_cmp_ge_i32 s3, s42
	s_waitcnt lgkmcnt(0)
	s_barrier
	s_cbranch_scc1 .LBB0_1072
	s_load_dwordx8 s[12:19], s[20:21], 0x118
	s_movk_i32 s46, 0x80
	s_load_dwordx2 s[20:21], s[20:21], 0x230
	s_and_b32 s43, s2, 7
	v_and_or_b32 v1, v1, 12, v193
	v_and_or_b32 v135, v183, s46, v185
	s_mov_b32 s47, 0x1ffffc0
	s_mov_b64 s[22:23], 0x10000
	s_mov_b64 s[24:25], 0x20000
	s_mov_b64 s[26:27], 0x30000
	s_mov_b64 s[28:29], 0x40000
	s_mov_b64 s[30:31], 0x50000
	s_mov_b64 s[36:37], 0x60000
	s_mov_b64 s[38:39], 0x70000

; __device__ __forceinline__ unsigned xb_ld(unsigned* p)              { return __hip_atomic_load(p, __ATOMIC_RELAXED, __HIP_MEMORY_SCOPE_AGENT); }
; __device__ __forceinline__ unsigned xb_add(unsigned* p, unsigned v) { return __hip_atomic_fetch_add(p, v, __ATOMIC_RELAXED, __HIP_MEMORY_SCOPE_AGENT); }
; #define XB_SPIN(cond, bar) do { unsigned _sp = 0; while (cond) { __builtin_amdgcn_s_sleep(1); \
;     if ((++_sp & 255u) == 0u) { if (xb_ld(&(bar)[XB_TMO])) break; if (_sp > XB_SPIN_CAP) { atomicAdd(&(bar)[XB_TMO], 1u); break; } } } } while (0)
; __device__ __forceinline__ void xcd_barrier(const XcdBarrier& b) {
;   asm volatile("s_waitcnt vmcnt(0)" ::: "memory");
;   __syncthreads();
;   if (threadIdx.x == 0) {
;     unsigned* bar = b.bar;
;     __builtin_amdgcn_s_waitcnt(0);
;     unsigned nloc = b.st[0], nx = b.st[1];
;     if (nloc == 0u) { xcd_barrier_complete(bar, b.x, nloc, nx); b.st[0] = nloc; b.st[1] = nx; }
;     const unsigned old = xb_add(&bar[XB_XSUB(b.x)], 1u);
;     const unsigned gen = old / nloc;
;     if (old + 1u == (gen + 1u) * nloc) {
;       __builtin_amdgcn_fence(__ATOMIC_RELEASE, "agent");
;       asm volatile("s_waitcnt vmcnt(0)" ::: "memory");
;       const unsigned og = xb_add(&bar[XB_TOP], 1u);
;       const unsigned tg = og / nx;
;       if (og + 1u == (tg + 1u) * nx) xb_add(&bar[XB_TOPGEN], 1u);
;       else XB_SPIN(xb_ld(&bar[XB_TOPGEN]) == tg, bar);
;       __builtin_amdgcn_fence(__ATOMIC_ACQUIRE, "agent");
;       xb_add(&bar[XB_XGEN(b.x)], 1u);
;       asm volatile("s_waitcnt vmcnt(0)" ::: "memory");
;     } else {
;       XB_SPIN(xb_ld(&bar[XB_XGEN(b.x)]) == gen, bar);
;       __builtin_amdgcn_fence(__ATOMIC_ACQUIRE, "agent");
;       asm volatile("s_waitcnt vmcnt(0)" ::: "memory");
;     }
;   }
;   __syncthreads();
; }
.LBB0_1072:
	s_waitcnt vmcnt(0)
	s_waitcnt vmcnt(63) expcnt(7) lgkmcnt(15)
	s_barrier
	s_and_saveexec_b64 s[12:13], s[4:5]
	s_cbranch_execz .LBB0_1124
	s_waitcnt vmcnt(0) lgkmcnt(0)
	s_add_u32 s98, s98, 1
	v_mov_b32_e32 v253, 0x12810
	ds_read_b32 v254, v253
	ds_read_b32 v253, v253 offset:4
	s_lshl_b32 s101, s33, 8
	s_add_u32 s99, s101, 5120
	s_waitcnt lgkmcnt(0)
	v_readfirstlane_b32 s100, v254
	v_mov_b32_e32 v254, s99
	v_readfirstlane_b32 s99, v253
	s_nop 0
	v_mov_b32_e32 v253, v254
	v_mov_b32_e32 v254, 1
	global_atomic_add v254, v253, v254, s[44:45] offset:64 sc0
	buffer_inv sc1
	s_mul_i32 s100, s100, s98
	s_mul_i32 s99, s99, s98
	s_waitcnt vmcnt(0)
	v_add_u32_e32 v254, 1, v254
	v_cmp_ne_u32_e32 vcc, s100, v254
	s_cbranch_vccnz .Lgb_wait_8
	buffer_wbl2 sc1
	s_waitcnt vmcnt(0)
	v_mov_b32_e32 v254, 1
	v_mov_b32_e32 v253, 9216
	global_atomic_add v253, v254, s[44:45] offset:64
	global_atomic_add v253, v254, s[44:45] offset:320
	global_atomic_add v253, v254, s[44:45] offset:576
	global_atomic_add v253, v254, s[44:45] offset:832
	global_atomic_add v253, v254, s[44:45] offset:1088
	global_atomic_add v253, v254, s[44:45] offset:1344
	global_atomic_add v253, v254, s[44:45] offset:1600
	global_atomic_add v253, v254, s[44:45] offset:1856
	v_mov_b32_e32 v253, 11264
	global_atomic_add v253, v254, s[44:45] offset:64
	global_atomic_add v253, v254, s[44:45] offset:320
	global_atomic_add v253, v254, s[44:45] offset:576
	global_atomic_add v253, v254, s[44:45] offset:832
	global_atomic_add v253, v254, s[44:45] offset:1088
	global_atomic_add v253, v254, s[44:45] offset:1344
	global_atomic_add v253, v254, s[44:45] offset:1600
	global_atomic_add v253, v254, s[44:45] offset:1856

; __device__ __forceinline__ float bflo(uint32_t w) { return __uint_as_float(w << 16); }
; __device__ __forceinline__ float bfhi(uint32_t w) { return __uint_as_float(w & 0xffff0000u); }
; __device__ void phase_postmix(KParams& p, int bid, int nb, char* smem) {
;   const int lane = threadIdx.x & 63, w = threadIdx.x >> 6;
;   for (int t = bid * 4 + w; t < T; t += nb * 4) {
;     const int b = t / L;
;     float4 y[8];
;     float ss = 0.f;
; #pragma unroll
;     for (int c = 0; c < 8; ++c) {
;       {
;         const uint2 yq = *reinterpret_cast<const uint2*>(reinterpret_cast<const bf16_t*>(p.y_x) + (size_t)t * D + c * 256 + lane * 4);
;         y[c] = float4{bflo(yq.x), bfhi(yq.x), bflo(yq.y), bfhi(yq.y)};
;       }
;       ss += y[c].x * y[c].x + y[c].y * y[c].y + y[c].z * y[c].z + y[c].w * y[c].w;
;     }
;     ss = wave_sum_fast(ss);
;     const float rstd = rsqrtf(ss * (1.f / D) + EPS);
;     const float* gm = p.mod + (size_t)b * NMOD + 2 * D;
;     float ss1 = 0.f;
; #pragma unroll
;     for (int c = 0; c < 8; ++c) {
;       const int e0 = c * 256 + lane * 4;
;       const float4 xv = *reinterpret_cast<const float4*>(p.x + (size_t)t * D + e0);
;       const float4 g4 = *reinterpret_cast<const float4*>(gm + e0), gp = *reinterpret_cast<const float4*>(p.g_post_mix + e0);
;       y[c].x = xv.x + g4.x * (y[c].x * rstd * gp.x); y[c].y = xv.y + g4.y * (y[c].y * rstd * gp.y);
;       y[c].z = xv.z + g4.z * (y[c].z * rstd * gp.z); y[c].w = xv.w + g4.w * (y[c].w * rstd * gp.w);
;       ss1 += y[c].x * y[c].x + y[c].y * y[c].y + y[c].z * y[c].z + y[c].w * y[c].w;
;     }
;     if (lane == 0) p.partial[t] = rstd;
.Lgb_wd_8:
.LBB0_1124:
	s_or_b64 exec, exec, s[12:13]
	s_mov_b64 s[24:25], s[0:1]
	s_waitcnt lgkmcnt(0)
	s_barrier
	s_and_saveexec_b64 s[20:21], s[6:7]
	s_cbranch_execz .LBB0_1131
	s_load_dwordx2 s[26:27], s[24:25], 0x230
	s_load_dwordx4 s[12:15], s[24:25], 0x180
	s_load_dwordx2 s[28:29], s[24:25], 0xf8
	s_load_dwordx2 s[30:31], s[24:25], 0x0
	s_load_dwordx4 s[16:19], s[24:25], 0x38
	s_load_dwordx2 s[36:37], s[24:25], 0x118
	s_load_dwordx2 s[22:23], s[24:25], 0x108
	v_mov_b32_e32 v135, 0
	v_or_b32_e32 v8, 0x400, v190
	v_lshlrev_b32_e32 v10, 2, v8
	v_mov_b32_e32 v11, v135
	s_waitcnt lgkmcnt(0)
	v_lshl_add_u64 v[102:103], s[16:17], 0, v[10:11]
	v_or_b32_e32 v12, 0x500, v190
	v_or_b32_e32 v16, 0x600, v190
	v_or_b32_e32 v20, 0x700, v190
	v_lshl_add_u64 v[112:113], s[18:19], 0, v[10:11]
	v_lshlrev_b64 v[10:11], 12, v[186:187]
	v_lshlrev_b32_e32 v14, 2, v12
	v_mov_b32_e32 v15, v135
	v_lshlrev_b32_e32 v18, 2, v16
	v_mov_b32_e32 v19, v135
	v_lshlrev_b32_e32 v22, 2, v20
	v_mov_b32_e32 v23, v135
	v_lshl_or_b32 v10, v184, 3, v10
	v_cmp_lt_i32_e32 vcc, v179, v180
	v_and_b32_e32 v3, 0xe0, v182
	v_lshlrev_b32_e32 v5, 4, v140
	v_and_b32_e32 v7, 12, v183
	v_lshl_add_u64 v[110:111], s[18:19], 0, v[134:135]
	v_lshl_add_u64 v[114:115], s[18:19], 0, v[14:15]
	v_lshl_add_u64 v[116:117], s[18:19], 0, v[18:19]
	v_lshl_add_u64 v[118:119], s[18:19], 0, v[22:23]
	v_lshl_add_u64 v[10:11], s[26:27], 0, v[10:11]
	s_mov_b64 s[18:19], 0xe00
	v_cndmask_b32_e32 v1, v178, v179, vcc
	v_cmp_lt_i32_e32 vcc, v181, v180
	v_lshl_add_u64 v[122:123], v[10:11], 0, s[18:19]
	v_or3_b32 v10, v3, v5, v7
	v_mov_b32_e32 v11, v135
	v_cndmask_b32_e32 v2, v178, v181, vcc
	v_lshl_add_u64 v[126:127], s[36:37], 0, v[10:11]
	v_lshlrev_b64 v[10:11], 13, v[186:187]
	v_lshlrev_b32_e32 v185, 2, v2
	s_lshl_b32 s24, s34, 2
	v_or_b32_e32 v2, 0x100, v190
	v_or_b32_e32 v4, 0x200, v190
	v_or_b32_e32 v6, 0x300, v190
	v_or_b32_e32 v10, v10, v188
	v_lshl_add_u64 v[98:99], s[28:29], 0, v[190:191]
	s_ashr_i32 s25, s24, 31
	v_lshl_add_u64 v[10:11], s[30:31], 0, v[10:11]
	s_mov_b64 s[28:29], 0x1c0c
	v_lshlrev_b32_e32 v130, 2, v2
	v_lshlrev_b32_e32 v136, 2, v4
	v_lshlrev_b32_e32 v140, 2, v6
	v_lshlrev_b32_e32 v144, 2, v8
	v_lshlrev_b32_e32 v148, 2, v12
	v_lshlrev_b32_e32 v152, 2, v16
	v_lshlrev_b32_e32 v156, 2, v20
	v_lshlrev_b32_e32 v1, 2, v1
	v_lshl_add_u64 v[100:101], s[16:17], 0, v[134:135]
	v_lshl_add_u64 v[104:105], s[16:17], 0, v[14:15]
	v_lshl_add_u64 v[106:107], s[16:17], 0, v[18:19]
	v_lshl_add_u64 v[108:109], s[16:17], 0, v[22:23]
	v_lshlrev_b64 v[120:121], 2, v[186:187]
	s_lshl_b64 s[16:17], s[24:25], 2
	s_lshl_b64 s[18:19], s[24:25], 12
	v_lshlrev_b64 v[124:125], 11, v[186:187]
	s_lshl_b64 s[26:27], s[24:25], 11
	v_lshl_add_u64 v[128:129], v[10:11], 0, s[28:29]
	s_lshl_b64 s[28:29], s[24:25], 13
	s_mov_b64 s[30:31], 0
	v_mov_b32_e32 v183, 0x358637bd
	s_mov_b32 s3, 0x800000
	s_mov_b64 s[36:37], 0x4000
	s_movk_i32 s25, 0xf000
	v_mov_b32_e32 v132, v130
	v_mov_b32_e32 v133, v135
	v_mov_b32_e32 v138, v136
	v_mov_b32_e32 v139, v135
	v_mov_b32_e32 v142, v140
	v_mov_b32_e32 v143, v135
	v_mov_b32_e32 v146, v144
	v_mov_b32_e32 v147, v135
	v_mov_b32_e32 v150, v148
	v_mov_b32_e32 v151, v135
	v_mov_b32_e32 v154, v152
	v_mov_b32_e32 v155, v135
	v_mov_b32_e32 v158, v156
	v_mov_b32_e32 v159, v135
	s_mov_b64 s[38:39], 0x6000
	s_mov_b64 s[40:41], 0x8000
	s_mov_b32 s35, 0x42ee0000
	s_mov_b32 s46, 0xc0c0500
	s_mov_b32 s47, 0xff0000
	s_mov_b32 s50, 0x80808080
	s_mov_b32 s51, 0x8080808
	s_mov_b32 s52, 0xf0f0f0f
	s_movk_i32 s53, 0x1fff
	v_mov_b32_e32 v191, 0xf0f0f0f
	v_mov_b32_e32 v192, v186
	s_branch .LBB0_1127

; __device__ __forceinline__ unsigned xb_ld(unsigned* p)              { return __hip_atomic_load(p, __ATOMIC_RELAXED, __HIP_MEMORY_SCOPE_AGENT); }
; __device__ __forceinline__ unsigned xb_add(unsigned* p, unsigned v) { return __hip_atomic_fetch_add(p, v, __ATOMIC_RELAXED, __HIP_MEMORY_SCOPE_AGENT); }
; #define XB_SPIN(cond, bar) do { unsigned _sp = 0; while (cond) { __builtin_amdgcn_s_sleep(1); \
;     if ((++_sp & 255u) == 0u) { if (xb_ld(&(bar)[XB_TMO])) break; if (_sp > XB_SPIN_CAP) { atomicAdd(&(bar)[XB_TMO], 1u); break; } } } } while (0)
; __device__ __forceinline__ void xcd_barrier(const XcdBarrier& b) {
;   asm volatile("s_waitcnt vmcnt(0)" ::: "memory");
;   __syncthreads();
;   if (threadIdx.x == 0) {
;     unsigned* bar = b.bar;
;     __builtin_amdgcn_s_waitcnt(0);
;     unsigned nloc = b.st[0], nx = b.st[1];
;     if (nloc == 0u) { xcd_barrier_complete(bar, b.x, nloc, nx); b.st[0] = nloc; b.st[1] = nx; }
;     const unsigned old = xb_add(&bar[XB_XSUB(b.x)], 1u);
;     const unsigned gen = old / nloc;
;     if (old + 1u == (gen + 1u) * nloc) {
;       __builtin_amdgcn_fence(__ATOMIC_RELEASE, "agent");
;       asm volatile("s_waitcnt vmcnt(0)" ::: "memory");
;       const unsigned og = xb_add(&bar[XB_TOP], 1u);
;       const unsigned tg = og / nx;
;       if (og + 1u == (tg + 1u) * nx) xb_add(&bar[XB_TOPGEN], 1u);
;       else XB_SPIN(xb_ld(&bar[XB_TOPGEN]) == tg, bar);
;       __builtin_amdgcn_fence(__ATOMIC_ACQUIRE, "agent");
;       xb_add(&bar[XB_XGEN(b.x)], 1u);
;       asm volatile("s_waitcnt vmcnt(0)" ::: "memory");
;     } else {
;       XB_SPIN(xb_ld(&bar[XB_XGEN(b.x)]) == gen, bar);
;       __builtin_amdgcn_fence(__ATOMIC_ACQUIRE, "agent");
;       asm volatile("s_waitcnt vmcnt(0)" ::: "memory");
;     }
;   }
;   __syncthreads();
; }
.LBB0_1131:
	s_or_b64 exec, exec, s[20:21]
	s_waitcnt vmcnt(0)
	s_barrier
	s_and_saveexec_b64 s[8:9], s[4:5]
	s_cbranch_execz .LBB0_1183
	s_waitcnt vmcnt(0) lgkmcnt(0)
	s_add_u32 s98, s98, 1
	v_mov_b32_e32 v253, 0x12810
	ds_read_b32 v254, v253
	ds_read_b32 v253, v253 offset:4
	s_lshl_b32 s101, s33, 8
	s_add_u32 s99, s101, 5120
	s_waitcnt lgkmcnt(0)
	v_readfirstlane_b32 s100, v254
	v_mov_b32_e32 v254, s99
	v_readfirstlane_b32 s99, v253
	s_nop 0
	v_mov_b32_e32 v253, v254
	v_mov_b32_e32 v254, 1
	global_atomic_add v254, v253, v254, s[44:45] offset:64 sc0
	buffer_inv sc1
	s_mul_i32 s100, s100, s98
	s_mul_i32 s99, s99, s98
	s_waitcnt vmcnt(0)
	v_add_u32_e32 v254, 1, v254
	v_cmp_ne_u32_e32 vcc, s100, v254
	s_cbranch_vccnz .Lgb_wait_9
	buffer_wbl2 sc1
	s_waitcnt vmcnt(0)
	v_mov_b32_e32 v254, 1
	v_mov_b32_e32 v253, 9216
	global_atomic_add v253, v254, s[44:45] offset:64
	global_atomic_add v253, v254, s[44:45] offset:320
	global_atomic_add v253, v254, s[44:45] offset:576
	global_atomic_add v253, v254, s[44:45] offset:832
	global_atomic_add v253, v254, s[44:45] offset:1088
	global_atomic_add v253, v254, s[44:45] offset:1344
	global_atomic_add v253, v254, s[44:45] offset:1600
	global_atomic_add v253, v254, s[44:45] offset:1856
	v_mov_b32_e32 v253, 11264
	global_atomic_add v253, v254, s[44:45] offset:64
	global_atomic_add v253, v254, s[44:45] offset:320
	global_atomic_add v253, v254, s[44:45] offset:576
	global_atomic_add v253, v254, s[44:45] offset:832
	global_atomic_add v253, v254, s[44:45] offset:1088
	global_atomic_add v253, v254, s[44:45] offset:1344
	global_atomic_add v253, v254, s[44:45] offset:1600
	global_atomic_add v253, v254, s[44:45] offset:1856

; __device__ __forceinline__ int opaque_tid() { int t = threadIdx.x; asm volatile("" : "+v"(t)); return t; }
; __device__ void phase_q_route(KParams& p, int bid, int nb, char* smem) {
;   const int tid = opaque_tid(), lane = tid & 63, w = tid >> 6;
;   const int wm = w >> 1, wn = w & 1, lr = lane & 15, lq = lane >> 4;
;   const int l31 = lane & 31, lh = lane >> 5;
;   for (int tile0 = bid; tile0 < 512; tile0 += nb) {
;     const int tile = ((nb & 7) == 0 && nb >= 512) ? (((tile0 & 7) * 8 + ((tile0 >> 3) & 7)) * 8 + (tile0 >> 6)) : tile0;
;     const int h = tile & 7, m0 = (tile >> 3) * 128;
;     {
;       f32x4 acc[4][4];
;       gemm_mainloop<true>(reinterpret_cast<const bf16_t*>(p.hx8a), D / 2, reinterpret_cast<const bf16_t*>(p.wq8), D / 2, D / 2, m0, h * 128, acc, smem);
; #pragma unroll
;       for (int i = 0; i < 4; ++i) {
;         const float4 rs = *reinterpret_cast<const float4*>(p.ascale + m0 + wm * 64 + i * 16 + lq * 4);
; #pragma unroll
;         for (int j = 0; j < 4; ++j) {
;           typedef __attribute__((ext_vector_type(4))) int i32x4;
;           const i32x4 ia = __builtin_bit_cast(i32x4, acc[i][j]);
;           const float cs = p.wqscale[h * 128 + wn * 64 + j * 16 + lr];
;           const float qv[4] = {(float)ia[0] * rs.x * cs, (float)ia[1] * rs.y * cs, (float)ia[2] * rs.z * cs, (float)ia[3] * rs.w * cs};
; #pragma unroll
;           for (int r = 0; r < 4; ++r) {
;             const int row = wm * 64 + i * 16 + lq * 4 + r, col = wn * 64 + j * 16 + lr;
;             *reinterpret_cast<bf16_t*>(smem + swz16(row, col >> 3) + (col & 7) * 2) = f2bf(qv[r]);
;           }
;         }
;       }
;     }
; #pragma unroll 4
;     for (int r = 0; r < 16; ++r) {
;       const int id = tid + 256 * r, row = id >> 4, c4 = id & 15;
;       const float* src = ((row < 128) ? p.sk1 : p.sk2) + ((size_t)(h * 128 + (row & 127)) * 64 + c4 * 4);
;       const float4 v = *reinterpret_cast<const float4*>(src);
;       uint2 pk; pk.x = pack2(v.x, v.y); pk.y = pack2(v.z, v.w);
;       *reinterpret_cast<uint2*>(smem + 32768 + swz8(row, c4 >> 1) + (c4 & 1) * 8) = pk;
;     }
;     __syncthreads();
;     uint32_t L1[16], L2[16];
.Lgb_wd_9:
.LBB0_1183:
	s_or_b64 exec, exec, s[8:9]
	s_mov_b64 s[10:11], s[0:1]
	s_waitcnt lgkmcnt(0)
	v_mov_b32_e32 v1, v0
	s_cmpk_gt_i32 s2, 0x1ff
	s_barrier
	s_cbranch_scc1 .LBB0_1196
	s_load_dwordx2 s[20:21], s[10:11], 0xf8
	s_load_dwordx2 s[12:13], s[10:11], 0x108
	v_ashrrev_i32_e32 v2, 1, v1
	s_cmpk_gt_i32 s34, 0x1ff
	v_and_b32_e32 v2, 0xffffffc0, v2
	v_and_b32_e32 v6, 63, v1
	s_cselect_b64 s[8:9], -1, 0
	v_ashrrev_i32_e32 v3, 31, v2
	s_and_b64 s[22:23], s[8:9], s[48:49]
	s_waitcnt lgkmcnt(0)
	v_lshl_add_u64 v[4:5], v[2:3], 2, s[12:13]
	v_lshrrev_b32_e32 v3, 2, v1
	v_cmp_lt_u32_e64 s[8:9], 31, v6
	v_lshrrev_b32_e32 v6, 3, v1
	v_and_b32_e32 v8, 31, v1
	v_ashrrev_i32_e32 v10, 6, v1
	v_and_b32_e32 v11, 12, v3
	v_lshlrev_b32_e32 v12, 3, v1
	s_movk_i32 s3, 0x1100
	v_and_b32_e32 v6, 9, v6
	v_or_b32_e32 v2, v11, v2
	v_and_b32_e32 v76, 8, v12
	v_lshlrev_b32_e32 v12, 8, v8
	v_mul_lo_u32 v14, v10, s3
	s_movk_i32 s3, 0x88
	s_load_dwordx4 s[12:15], s[10:11], 0x138
	s_load_dwordx4 s[16:19], s[10:11], 0x240
	v_or_b32_e32 v16, 2, v6
	v_or_b32_e32 v20, 4, v6
	v_or_b32_e32 v24, 6, v6
	v_bfe_u32 v7, v1, 5, 1
	v_and_b32_e32 v9, 15, v1
	v_lshlrev_b32_e32 v66, 2, v11
	v_mov_b32_e32 v67, 0
	v_lshl_or_b32 v12, v10, 13, v12
	v_and_b32_e32 v13, 7, v1
	v_mad_u32_u24 v78, v8, s3, v14
	v_lshl_or_b32 v79, v10, 5, v8
	v_lshlrev_b32_e32 v2, 8, v2
	v_bitop3_b32 v3, v3, v6, 12 bitop3:0x6c
	v_bitop3_b32 v10, v11, v6, 1 bitop3:0x36
	v_bitop3_b32 v14, v11, v6, 2 bitop3:0x36
	v_bitop3_b32 v15, v11, v6, 3 bitop3:0x36
	v_bitop3_b32 v17, v6, v11, 2 bitop3:0x36
	v_bitop3_b32 v18, v11, v16, 1 bitop3:0x36
	v_bitop3_b32 v19, v11, v6, 2 bitop3:0x14
	v_bitop3_b32 v16, v11, v16, 3 bitop3:0x36
	v_bitop3_b32 v21, v6, v11, 4 bitop3:0x36
	v_bitop3_b32 v22, v11, v20, 1 bitop3:0x36
	v_bitop3_b32 v23, v11, v20, 2 bitop3:0x36
	v_bitop3_b32 v20, v11, v20, 3 bitop3:0x36
	v_bitop3_b32 v6, v6, v11, 6 bitop3:0x36
	v_bitop3_b32 v25, v11, v24, 1 bitop3:0x36
	v_bitop3_b32 v26, v11, v24, 2 bitop3:0x36
	v_bitop3_b32 v11, v11, v24, 3 bitop3:0x36
	v_lshl_add_u64 v[68:69], v[4:5], 0, v[66:67]
	v_lshlrev_b32_e32 v4, 1, v1
	v_lshlrev_b32_e32 v77, 2, v7
	v_lshl_or_b32 v3, v3, 4, v2
	v_lshl_or_b32 v10, v10, 4, v2
	v_lshl_or_b32 v14, v14, 4, v2
	v_lshl_or_b32 v15, v15, 4, v2
	v_lshl_or_b32 v17, v17, 4, v2
	v_lshl_or_b32 v18, v18, 4, v2
	v_lshl_or_b32 v19, v19, 4, v2
	v_lshl_or_b32 v16, v16, 4, v2
	v_lshl_or_b32 v21, v21, 4, v2
	v_lshl_or_b32 v22, v22, 4, v2
	v_lshl_or_b32 v23, v23, 4, v2
	v_lshl_or_b32 v20, v20, 4, v2
	v_lshl_or_b32 v6, v6, 4, v2
	v_lshl_or_b32 v25, v25, 4, v2
	v_lshl_or_b32 v26, v26, 4, v2
	v_lshl_or_b32 v2, v11, 4, v2
	v_bitop3_b32 v11, v7, v1, 15 bitop3:0x78
	v_bitop3_b32 v24, v7, v1, 7 bitop3:0x78
	v_bitop3_b32 v27, v7, v9, 2 bitop3:0x36
	v_bitop3_b32 v28, v7, v13, 2 bitop3:0x36
	v_bitop3_b32 v29, v7, v9, 4 bitop3:0x36
	v_bitop3_b32 v30, v7, v13, 4 bitop3:0x36
	v_bitop3_b32 v31, v7, v9, 6 bitop3:0x36
	v_bitop3_b32 v13, v7, v13, 6 bitop3:0x36
	v_bitop3_b32 v32, v7, v9, 8 bitop3:0x36
	v_bitop3_b32 v33, v7, v9, 10 bitop3:0x36
	v_bitop3_b32 v34, v7, v9, 12 bitop3:0x36
	v_bitop3_b32 v7, v7, v9, 14 bitop3:0x36
	v_and_b32_e32 v4, 14, v4
	v_lshlrev_b32_e32 v5, 2, v9
	v_lshlrev_b32_e32 v8, 7, v8
	v_lshlrev_b32_e32 v11, 4, v11
	v_lshlrev_b32_e32 v24, 4, v24
	v_lshlrev_b32_e32 v27, 4, v27
	v_lshlrev_b32_e32 v28, 4, v28
	v_lshlrev_b32_e32 v29, 4, v29
	v_lshlrev_b32_e32 v30, 4, v30
	v_lshlrev_b32_e32 v31, 4, v31
	v_lshlrev_b32_e32 v13, 4, v13
	v_lshlrev_b32_e32 v32, 4, v32
	v_lshlrev_b32_e32 v33, 4, v33
	v_lshlrev_b32_e32 v34, 4, v34
	v_lshlrev_b32_e32 v7, 4, v7
	v_and_b32_e32 v74, 0x4f, v1
	v_bfe_u32 v75, v1, 1, 3
	v_or_b32_e32 v80, 1, v77
	v_or_b32_e32 v81, 2, v77
	v_or_b32_e32 v82, 3, v77
	v_or_b32_e32 v83, 8, v77
	v_or_b32_e32 v84, 9, v77
	v_or_b32_e32 v85, 10, v77
	v_or_b32_e32 v86, 11, v77
	v_or_b32_e32 v87, 16, v77
	v_or_b32_e32 v88, 17, v77
	v_or_b32_e32 v89, 18, v77
	v_or_b32_e32 v90, 19, v77
	v_or_b32_e32 v91, 24, v77
	v_or_b32_e32 v92, 25, v77
	v_or_b32_e32 v93, 26, v77
	v_or_b32_e32 v94, 27, v77
	v_or_b32_e32 v95, 32, v77
	v_or_b32_e32 v96, 33, v77
	v_or_b32_e32 v97, 35, v77
	v_or_b32_e32 v98, 34, v77
	v_or_b32_e32 v99, 43, v77
	v_or_b32_e32 v100, 42, v77
	v_or_b32_e32 v101, 40, v77
	v_or_b32_e32 v102, 41, v77
	v_or_b32_e32 v103, 59, v77
	v_or_b32_e32 v104, 58, v77
	v_or_b32_e32 v105, 56, v77
	v_or_b32_e32 v106, 57, v77
	v_or_b32_e32 v107, 48, v77
	v_or_b32_e32 v108, 49, v77
	v_or_b32_e32 v109, 51, v77
	v_or_b32_e32 v110, 50, v77
	v_or_b32_e32 v111, 64, v77
	v_or_b32_e32 v112, 0x41, v77
	v_or_b32_e32 v113, 0x43, v77
	v_or_b32_e32 v114, 0x42, v77
	v_or_b32_e32 v115, 0x4b, v77
	v_or_b32_e32 v116, 0x4a, v77
	v_or_b32_e32 v117, 0x48, v77
	v_or_b32_e32 v118, 0x49, v77
	v_or_b32_e32 v119, 0x5b, v77
	v_or_b32_e32 v120, 0x5a, v77
	v_or_b32_e32 v121, 0x58, v77
	v_or_b32_e32 v122, 0x59, v77
	v_or_b32_e32 v123, 0x50, v77
	v_or_b32_e32 v124, 0x51, v77
	v_or_b32_e32 v125, 0x53, v77
	v_or_b32_e32 v126, 0x52, v77
	v_or_b32_e32 v127, 0x60, v77
	v_or_b32_e32 v128, 0x61, v77
	v_or_b32_e32 v129, 0x63, v77
	v_or_b32_e32 v130, 0x62, v77
	v_or_b32_e32 v131, 0x6b, v77
	v_or_b32_e32 v132, 0x6a, v77
	v_or_b32_e32 v133, 0x68, v77
	v_or_b32_e32 v134, 0x69, v77
	v_or_b32_e32 v135, 0x7b, v77
	v_or_b32_e32 v136, 0x7a, v77
	v_or_b32_e32 v137, 0x78, v77
	v_or_b32_e32 v138, 0x79, v77
	v_or_b32_e32 v139, 0x70, v77
	v_or_b32_e32 v140, 0x71, v77
	v_or_b32_e32 v141, 0x73, v77
	v_or_b32_e32 v142, 0x72, v77
	s_movk_i32 s3, 0xff80
	s_mov_b64 s[24:25], 0x10000
	s_mov_b64 s[26:27], 0x20000
	s_mov_b64 s[28:29], 0x30000
	s_mov_b32 s35, 0x1ffffc0
	s_mov_b64 s[30:31], 0x80
	s_mov_b64 s[36:37], 0x10080
	s_mov_b64 s[38:39], 0x20080
	s_mov_b64 s[40:41], 0x30080
	v_add_u32_e32 v143, v3, v4
	v_add_u32_e32 v144, v10, v4
	v_add_u32_e32 v145, v14, v4
	v_add_u32_e32 v146, v15, v4
	v_add_u32_e32 v147, v17, v4
	v_add_u32_e32 v148, v18, v4
	v_add_u32_e32 v149, v19, v4
	v_add_u32_e32 v150, v16, v4
	v_add_u32_e32 v151, v21, v4
	v_add_u32_e32 v152, v22, v4
	v_add_u32_e32 v153, v23, v4
	v_add_u32_e32 v154, v20, v4
	v_add_u32_e32 v155, v6, v4
	v_add_u32_e32 v156, v25, v4
	v_add_u32_e32 v157, v26, v4
	v_add_u32_e32 v158, v2, v4
	s_movk_i32 s46, 0x80
	v_lshlrev_b32_e32 v159, 2, v5
	v_add_u32_e32 v160, v12, v11
	v_add_u32_e32 v161, v24, v8
	v_add_u32_e32 v162, v12, v27
	v_add_u32_e32 v163, v28, v8
	v_add_u32_e32 v164, v12, v29
	v_add_u32_e32 v165, v30, v8
	v_add_u32_e32 v166, v12, v31
	v_add_u32_e32 v167, v13, v8
	v_add_u32_e32 v168, v12, v32
	v_add_u32_e32 v169, v12, v33
	v_add_u32_e32 v170, v12, v34
	v_add_u32_e32 v171, v12, v7
	s_movk_i32 s47, 0xff00
	v_mov_b32_e32 v172, 0xc0
	v_mov_b32_e32 v173, 0xb8
	v_bfrev_b32_e32 v174, 1
	s_branch .LBB0_1186

; __device__ __forceinline__ unsigned xb_ld(unsigned* p)              { return __hip_atomic_load(p, __ATOMIC_RELAXED, __HIP_MEMORY_SCOPE_AGENT); }
; __device__ __forceinline__ unsigned xb_add(unsigned* p, unsigned v) { return __hip_atomic_fetch_add(p, v, __ATOMIC_RELAXED, __HIP_MEMORY_SCOPE_AGENT); }
; #define XB_SPIN(cond, bar) do { unsigned _sp = 0; while (cond) { __builtin_amdgcn_s_sleep(1); \
;     if ((++_sp & 255u) == 0u) { if (xb_ld(&(bar)[XB_TMO])) break; if (_sp > XB_SPIN_CAP) { atomicAdd(&(bar)[XB_TMO], 1u); break; } } } } while (0)
; __device__ __forceinline__ void xcd_barrier(const XcdBarrier& b) {
;   asm volatile("s_waitcnt vmcnt(0)" ::: "memory");
;   __syncthreads();
;   if (threadIdx.x == 0) {
;     unsigned* bar = b.bar;
;     __builtin_amdgcn_s_waitcnt(0);
;     unsigned nloc = b.st[0], nx = b.st[1];
;     if (nloc == 0u) { xcd_barrier_complete(bar, b.x, nloc, nx); b.st[0] = nloc; b.st[1] = nx; }
;     const unsigned old = xb_add(&bar[XB_XSUB(b.x)], 1u);
;     const unsigned gen = old / nloc;
;     if (old + 1u == (gen + 1u) * nloc) {
;       __builtin_amdgcn_fence(__ATOMIC_RELEASE, "agent");
;       asm volatile("s_waitcnt vmcnt(0)" ::: "memory");
;       const unsigned og = xb_add(&bar[XB_TOP], 1u);
;       const unsigned tg = og / nx;
;       if (og + 1u == (tg + 1u) * nx) xb_add(&bar[XB_TOPGEN], 1u);
;       else XB_SPIN(xb_ld(&bar[XB_TOPGEN]) == tg, bar);
;       __builtin_amdgcn_fence(__ATOMIC_ACQUIRE, "agent");
;       xb_add(&bar[XB_XGEN(b.x)], 1u);
;       asm volatile("s_waitcnt vmcnt(0)" ::: "memory");
;     } else {
;       XB_SPIN(xb_ld(&bar[XB_XGEN(b.x)]) == gen, bar);
;       __builtin_amdgcn_fence(__ATOMIC_ACQUIRE, "agent");
;       asm volatile("s_waitcnt vmcnt(0)" ::: "memory");
;     }
;   }
;   __syncthreads();
; }
.LBB0_1196:
	s_waitcnt vmcnt(0)
	s_barrier
	s_and_saveexec_b64 s[2:3], s[4:5]
	s_cbranch_execz .LBB0_1248
	s_waitcnt vmcnt(0) lgkmcnt(0)
	s_add_u32 s98, s98, 1
	v_mov_b32_e32 v253, 0x12810
	ds_read_b32 v254, v253
	ds_read_b32 v253, v253 offset:4
	s_lshl_b32 s101, s33, 8
	s_add_u32 s99, s101, 5120
	s_waitcnt lgkmcnt(0)
	v_readfirstlane_b32 s100, v254
	v_mov_b32_e32 v254, s99
	v_readfirstlane_b32 s99, v253
	s_nop 0
	v_mov_b32_e32 v253, v254
	v_mov_b32_e32 v254, 1
	global_atomic_add v254, v253, v254, s[44:45] offset:64 sc0
	buffer_inv sc1
	s_mul_i32 s100, s100, s98
	s_mul_i32 s99, s99, s98
	s_waitcnt vmcnt(0)
	v_add_u32_e32 v254, 1, v254
	v_cmp_ne_u32_e32 vcc, s100, v254
	s_cbranch_vccnz .Lgb_wait_10
	buffer_wbl2 sc1
	s_waitcnt vmcnt(0)
	v_mov_b32_e32 v254, 1
	v_mov_b32_e32 v253, 9216
	global_atomic_add v253, v254, s[44:45] offset:64
	global_atomic_add v253, v254, s[44:45] offset:320
	global_atomic_add v253, v254, s[44:45] offset:576
	global_atomic_add v253, v254, s[44:45] offset:832
	global_atomic_add v253, v254, s[44:45] offset:1088
	global_atomic_add v253, v254, s[44:45] offset:1344
	global_atomic_add v253, v254, s[44:45] offset:1600
	global_atomic_add v253, v254, s[44:45] offset:1856
	v_mov_b32_e32 v253, 11264
	global_atomic_add v253, v254, s[44:45] offset:64
	global_atomic_add v253, v254, s[44:45] offset:320
	global_atomic_add v253, v254, s[44:45] offset:576
	global_atomic_add v253, v254, s[44:45] offset:832
	global_atomic_add v253, v254, s[44:45] offset:1088
	global_atomic_add v253, v254, s[44:45] offset:1344
	global_atomic_add v253, v254, s[44:45] offset:1600
	global_atomic_add v253, v254, s[44:45] offset:1856

; __device__ __forceinline__ int opaque_tid() { int t = threadIdx.x; asm volatile("" : "+v"(t)); return t; }
; __device__ __forceinline__ unsigned my_xcc_id() { return (unsigned)__builtin_amdgcn_s_getreg((3 << 11) | 20) & 7u; }
; __device__ void phase_exp_u(KParams& p, char* smem) {
;   const int tid = opaque_tid(), lane = tid & 63, w = tid >> 6;
;   const int sub = lane >> 3, cc = lane & 7;
;   const unsigned myx = my_xcc_id();
;   int* sh = reinterpret_cast<int*>(smem);
;   int* si = reinterpret_cast<int*>(smem + 64) + w * 256;
;   float* pbuf = reinterpret_cast<float*>(p.ycat);
;   {
;     unsigned qcur = 0;
;     for (;;) {
;       __syncthreads();
;       if (tid == 0) {
;         int found = -1; unsigned fx = 0;
;         for (; qcur < 8; ++qcur) {
;           fx = (myx + qcur) & 7u;
;           const int c = (int)atomicAdd(&p.ctr[16 + fx], 1u);
;           if (c < 128) { found = c; break; }
;         }
;         sh[0] = found; sh[1] = (int)fx;
;       }
;       __syncthreads();
;       const int chunk = sh[0];
;       const unsigned x = (unsigned)sh[1];
;       if (chunk < 0) break;
;       int e0n = p.idx[(size_t)(chunk * 64 + w * 16) * 128 + lane], e1n = p.idx[(size_t)(chunk * 64 + w * 16) * 128 + 64 + lane];
;       uint4 hqn0 = *reinterpret_cast<const uint4*>(p.ycat8 + (size_t)(chunk * 64 + w * 16) * D + x * 256 + cc * 32);
;       uint4 hqn1 = *reinterpret_cast<const uint4*>(p.ycat8 + (size_t)(chunk * 64 + w * 16) * D + x * 256 + cc * 32 + 16);
.Lgb_wd_10:
.LBB0_1248:
	s_or_b64 exec, exec, s[2:3]
	s_mov_b64 s[8:9], s[0:1]
	v_mov_b32_e32 v2, v0
	s_waitcnt lgkmcnt(0)
	s_barrier
	s_getreg_b32 s35, hwreg(HW_REG_XCC_ID, 0, 4)
	s_load_dwordx2 s[10:11], s[8:9], 0x248
	s_load_dwordx2 s[36:37], s[8:9], 0x228
	s_load_dwordx2 s[28:29], s[8:9], 0x218
	s_load_dwordx2 s[24:25], s[8:9], 0xe0
	s_load_dwordx2 s[30:31], s[8:9], 0x118
	v_ashrrev_i32_e32 v1, 6, v2
	v_and_b32_e32 v3, 7, v2
	v_cmp_eq_u32_e64 s[2:3], 0, v2
	v_lshlrev_b32_e32 v5, 2, v2
	v_lshrrev_b32_e32 v2, 1, v2
	v_lshlrev_b32_e32 v4, 10, v1
	v_mov_b32_e32 v11, 0
	v_and_b32_e32 v10, 0xfc, v5
	v_lshlrev_b32_e32 v14, 5, v3
	v_and_b32_e32 v2, 28, v2
	s_waitcnt lgkmcnt(0)
	v_lshl_add_u64 v[12:13], s[10:11], 0, v[10:11]
	v_or_b32_e32 v44, v4, v10
	v_or_b32_e32 v10, v14, v2
	v_mov_b32_e32 v15, v11
	v_lshlrev_b32_e32 v45, 4, v3
	v_or_b32_e32 v46, v4, v2
	v_cmp_eq_u32_e64 s[8:9], 0, v3
	v_cmp_eq_u32_e64 s[10:11], 1, v3
	v_cmp_eq_u32_e64 s[12:13], 2, v3
	v_cmp_eq_u32_e64 s[14:15], 3, v3
	v_cmp_eq_u32_e64 s[16:17], 4, v3
	v_cmp_eq_u32_e64 s[18:19], 5, v3
	v_cmp_eq_u32_e64 s[20:21], 6, v3
	v_cmp_eq_u32_e64 s[22:23], 7, v3
	v_lshl_add_u64 v[2:3], s[36:37], 0, v[10:11]
	s_mov_b64 s[36:37], 0x100
	v_lshlrev_b32_e32 v1, 4, v1
	s_mov_b32 s27, 0x20000
	s_brev_b32 s26, 64
	s_and_b32 s25, s25, 0xffff
	v_lshl_add_u64 v[16:17], s[30:31], 0, v[14:15]
	v_lshl_add_u64 v[18:19], v[2:3], 0, s[36:37]
	v_mov_b32_e32 v47, 1
	s_movk_i32 s46, 0x7f
	s_mov_b32 s47, 0
	s_mov_b64 s[36:37], 0x200
	v_mov_b32_e32 v48, 0
	s_branch .LBB0_1250

; __device__ void phase_exp_combine(KParams& p, int bid, int nb) {
;   const int lane = threadIdx.x & 63, w = threadIdx.x >> 6;
;   const float* pbuf = reinterpret_cast<const float*>(p.ycat);
;   for (int t = bid * 4 + w; t < T; t += nb * 4) {
;     const int e0 = p.idx[(size_t)t * 128 + lane], e1 = p.idx[(size_t)t * 128 + 64 + lane];
;     const float* pb = pbuf + (size_t)t * 128;
;     float d0 = 0.f, d1 = 0.f;
; #pragma unroll
;     for (int xs = 0; xs < 8; ++xs) { d0 += pb[(size_t)xs * T * 128 + lane]; d1 += pb[(size_t)xs * T * 128 + 64 + lane]; }
;     const float hs = p.ascale[t];
;     d0 *= p.uscale[e0] * hs; d1 *= p.uscale[e1] * hs;
;     const float g0 = p.gate[(size_t)t * 128 + lane], g1 = p.gate[(size_t)t * 128 + 64 + lane];
.Lgb_wd_11:
.LBB0_1316:
	s_or_b64 exec, exec, s[2:3]
	s_mov_b64 s[10:11], s[0:1]
	s_waitcnt lgkmcnt(0)
	s_barrier
	s_and_saveexec_b64 s[2:3], s[6:7]
	s_cbranch_execz .LBB0_1327
	s_load_dwordx2 s[12:13], s[10:11], 0x108
	s_load_dwordx2 s[14:15], s[10:11], 0x228
	s_load_dwordx2 s[8:9], s[10:11], 0xf0
	s_load_dwordx4 s[16:19], s[10:11], 0x240
	s_lshl_b32 s10, s34, 2
	v_lshlrev_b64 v[8:9], 9, v[186:187]
	s_ashr_i32 s11, s10, 31
	s_waitcnt lgkmcnt(0)
	v_lshl_add_u64 v[2:3], v[186:187], 2, s[12:13]
	v_lshl_add_u64 v[6:7], s[18:19], 0, v[8:9]
	s_mov_b64 s[18:19], 0x100
	s_lshl_b64 s[12:13], s[10:11], 2
	v_mov_b32_e32 v191, 0
	v_lshl_add_u64 v[4:5], s[14:15], 0, v[8:9]
	s_lshl_b64 s[14:15], s[10:11], 9
	v_lshl_add_u64 v[6:7], v[6:7], 0, s[18:19]
	v_lshl_add_u64 v[8:9], s[16:17], 0, v[8:9]
	s_mov_b64 s[16:17], 0
	s_mov_b32 s11, 0x400000
	s_mov_b32 s20, 0x800000
	s_mov_b32 s21, 0xc00000
	s_mov_b32 s22, 0x1000000
	s_mov_b32 s23, 0x1400000
	s_mov_b32 s24, 0x1800000
	s_mov_b32 s25, 0x1c00000
	s_mov_b32 s26, 0x378e98ab
	s_mov_b32 s27, 0x3b7cd369
	s_mov_b32 s28, 0xbcc618b2
	s_mov_b32 s29, 0x3dda74e4
	s_mov_b32 s30, 0x3f228afd
	s_mov_b32 s31, 0x3e03c728
	s_mov_b32 s35, 0xbfb8aa3b
	s_mov_b32 s36, 0x42ce8ed0
	s_mov_b32 s37, 0xc2b17218
	v_mov_b32_e32 v1, 0x3ba10414
	s_brev_b32 s38, -2
	s_movk_i32 s39, 0x1fff
	v_mov_b32_e32 v14, 0xb9c68948
	v_mov_b32_e32 v15, 0x7f800000
	v_mov_b32_e32 v16, v186
	s_branch .LBB0_1319

; __device__ __forceinline__ unsigned xb_ld(unsigned* p)              { return __hip_atomic_load(p, __ATOMIC_RELAXED, __HIP_MEMORY_SCOPE_AGENT); }
; __device__ __forceinline__ unsigned xb_add(unsigned* p, unsigned v) { return __hip_atomic_fetch_add(p, v, __ATOMIC_RELAXED, __HIP_MEMORY_SCOPE_AGENT); }
; #define XB_SPIN(cond, bar) do { unsigned _sp = 0; while (cond) { __builtin_amdgcn_s_sleep(1); \
;     if ((++_sp & 255u) == 0u) { if (xb_ld(&(bar)[XB_TMO])) break; if (_sp > XB_SPIN_CAP) { atomicAdd(&(bar)[XB_TMO], 1u); break; } } } } while (0)
; __device__ __forceinline__ void xcd_barrier(const XcdBarrier& b) {
;   asm volatile("s_waitcnt vmcnt(0)" ::: "memory");
;   __syncthreads();
;   if (threadIdx.x == 0) {
;     unsigned* bar = b.bar;
;     __builtin_amdgcn_s_waitcnt(0);
;     unsigned nloc = b.st[0], nx = b.st[1];
;     if (nloc == 0u) { xcd_barrier_complete(bar, b.x, nloc, nx); b.st[0] = nloc; b.st[1] = nx; }
;     const unsigned old = xb_add(&bar[XB_XSUB(b.x)], 1u);
;     const unsigned gen = old / nloc;
;     if (old + 1u == (gen + 1u) * nloc) {
;       __builtin_amdgcn_fence(__ATOMIC_RELEASE, "agent");
;       asm volatile("s_waitcnt vmcnt(0)" ::: "memory");
;       const unsigned og = xb_add(&bar[XB_TOP], 1u);
;       const unsigned tg = og / nx;
;       if (og + 1u == (tg + 1u) * nx) xb_add(&bar[XB_TOPGEN], 1u);
;       else XB_SPIN(xb_ld(&bar[XB_TOPGEN]) == tg, bar);
;       __builtin_amdgcn_fence(__ATOMIC_ACQUIRE, "agent");
;       xb_add(&bar[XB_XGEN(b.x)], 1u);
;       asm volatile("s_waitcnt vmcnt(0)" ::: "memory");
;     } else {
;       XB_SPIN(xb_ld(&bar[XB_XGEN(b.x)]) == gen, bar);
;       __builtin_amdgcn_fence(__ATOMIC_ACQUIRE, "agent");
;       asm volatile("s_waitcnt vmcnt(0)" ::: "memory");
;     }
;   }
;   __syncthreads();
; }
.LBB0_1327:
	s_or_b64 exec, exec, s[2:3]
	s_waitcnt vmcnt(0)
	s_barrier
	s_and_saveexec_b64 s[2:3], s[4:5]
	s_cbranch_execz .LBB0_1379
	s_waitcnt vmcnt(0) lgkmcnt(0)
	s_add_u32 s98, s98, 1
	v_mov_b32_e32 v253, 0x12810
	ds_read_b32 v254, v253
	ds_read_b32 v253, v253 offset:4
	s_lshl_b32 s101, s33, 8
	s_add_u32 s99, s101, 5120
	s_waitcnt lgkmcnt(0)
	v_readfirstlane_b32 s100, v254
	v_mov_b32_e32 v254, s99
	v_readfirstlane_b32 s99, v253
	s_nop 0
	v_mov_b32_e32 v253, v254
	v_mov_b32_e32 v254, 1
	global_atomic_add v254, v253, v254, s[44:45] offset:64 sc0
	buffer_inv sc1
	s_mul_i32 s100, s100, s98
	s_mul_i32 s99, s99, s98
	s_waitcnt vmcnt(0)
	v_add_u32_e32 v254, 1, v254
	v_cmp_ne_u32_e32 vcc, s100, v254
	s_cbranch_vccnz .Lgb_wait_12
	buffer_wbl2 sc1
	s_waitcnt vmcnt(0)
	v_mov_b32_e32 v254, 1
	v_mov_b32_e32 v253, 9216
	global_atomic_add v253, v254, s[44:45] offset:64
	global_atomic_add v253, v254, s[44:45] offset:320
	global_atomic_add v253, v254, s[44:45] offset:576
	global_atomic_add v253, v254, s[44:45] offset:832
	global_atomic_add v253, v254, s[44:45] offset:1088
	global_atomic_add v253, v254, s[44:45] offset:1344
	global_atomic_add v253, v254, s[44:45] offset:1600
	global_atomic_add v253, v254, s[44:45] offset:1856
	v_mov_b32_e32 v253, 11264
	global_atomic_add v253, v254, s[44:45] offset:64
	global_atomic_add v253, v254, s[44:45] offset:320
	global_atomic_add v253, v254, s[44:45] offset:576
	global_atomic_add v253, v254, s[44:45] offset:832
	global_atomic_add v253, v254, s[44:45] offset:1088
	global_atomic_add v253, v254, s[44:45] offset:1344
	global_atomic_add v253, v254, s[44:45] offset:1600
	global_atomic_add v253, v254, s[44:45] offset:1856

; __device__ __forceinline__ int opaque_tid() { int t = threadIdx.x; asm volatile("" : "+v"(t)); return t; }
; __device__ __forceinline__ unsigned my_xcc_id() { return (unsigned)__builtin_amdgcn_s_getreg((3 << 11) | 20) & 7u; }
; __device__ void phase_exp_v(KParams& p, char* smem) {
;   const int tid = opaque_tid(), lane = tid & 63, w = tid >> 6;
;   const int sub = lane >> 3, cc = lane & 7;
;   const unsigned myx = my_xcc_id();
;   int* sh = reinterpret_cast<int*>(smem);
;   int* si = reinterpret_cast<int*>(smem + 64) + w * 256;
;   float* sc = reinterpret_cast<float*>(si + 128);
;   bf16_t* yfb = reinterpret_cast<bf16_t*>(p.y_x) + (size_t)T * D;
;   {
;     unsigned qcur = 0;
;     for (;;) {
;       __syncthreads();
;       if (tid == 0) {
;         int found = -1; unsigned fx = 0;
;         for (; qcur < 8; ++qcur) {
;           fx = (myx + qcur) & 7u;
;           const int c = (int)atomicAdd(&p.ctr[32 + fx], 1u);
;           if (c < 128) { found = c; break; }
;         }
;         sh[0] = found; sh[1] = (int)fx;
;       }
;       __syncthreads();
;       const int chunk = sh[0];
;       const unsigned x = (unsigned)sh[1];
;       if (chunk < 0) break;
;       int e0n = p.idx[(size_t)(chunk * 64 + w * 16) * 128 + lane], e1n = p.idx[(size_t)(chunk * 64 + w * 16) * 128 + 64 + lane];
;       float g0n = p.gate[(size_t)(chunk * 64 + w * 16) * 128 + lane], g1n = p.gate[(size_t)(chunk * 64 + w * 16) * 128 + 64 + lane];
.Lgb_wd_12:
.LBB0_1379:
	s_or_b64 exec, exec, s[2:3]
	s_mov_b64 s[14:15], s[0:1]
	s_waitcnt lgkmcnt(0)
	s_barrier
	s_getreg_b32 s35, hwreg(HW_REG_XCC_ID, 0, 4)
	s_load_dwordx4 s[8:11], s[14:15], 0x240
	s_load_dwordx2 s[18:19], s[14:15], 0x230
	s_load_dwordx2 s[16:17], s[14:15], 0x218
	s_load_dwordx2 s[12:13], s[14:15], 0xe8
	v_ashrrev_i32_e32 v1, 6, v0
	v_and_b32_e32 v3, 7, v0
	v_lshlrev_b32_e32 v4, 10, v1
	v_and_b32_e32 v44, 63, v0
	v_bfe_u32 v2, v0, 3, 3
	v_cmp_eq_u32_e64 s[2:3], 0, v0
	v_lshlrev_b32_e32 v55, 4, v3
	v_lshl_add_u32 v0, v1, 13, v4
	v_lshlrev_b32_e32 v3, 3, v3
	v_mov_b32_e32 v47, 0
	v_lshlrev_b32_e32 v45, 4, v1
	v_lshl_or_b32 v54, v44, 2, v4
	v_lshl_or_b32 v56, v2, 2, v4
	s_movk_i32 s20, 0x90
	v_mul_u32_u24_e32 v1, 0x90, v44
	v_mul_u32_u24_e32 v4, 0x90, v2
	v_or_b32_e32 v5, v0, v55
	v_lshlrev_b32_e32 v46, 3, v2
	v_lshl_or_b32 v46, v3, 3, v46
	s_mov_b32 s15, 0x20000
	s_brev_b32 s14, 64
	s_waitcnt lgkmcnt(0)
	s_and_b32 s13, s13, 0xffff
	v_mad_u32_u24 v57, v2, s20, v5
	v_lshl_add_u64 v[48:49], s[18:19], 0, v[46:47]
	v_mov_b32_e32 v58, 1
	s_movk_i32 s36, 0x7f
	s_mov_b32 s37, 0
	v_add_u32_e32 v59, v0, v1
	v_add_u32_e32 v60, v5, v4
	v_add_u32_e32 v61, 0x400, v56
	v_mov_b32_e32 v62, 0
	s_branch .LBB0_1381

; __device__ __forceinline__ float bflo(uint32_t w) { return __uint_as_float(w << 16); }
; __device__ __forceinline__ float bfhi(uint32_t w) { return __uint_as_float(w & 0xffff0000u); }
; __device__ void phase_exp_final(KParams& p, int bid, int nb, char* smem) {
;   const int lane = threadIdx.x & 63, w = threadIdx.x >> 6;
;   const bf16_t* ymix = reinterpret_cast<const bf16_t*>(p.y_x);
;   const bf16_t* yf = reinterpret_cast<const bf16_t*>(p.y_x) + (size_t)T * D;
;   for (int t = bid * 4 + w; t < T; t += nb * 4) {
;     const int b = t / L;
;     float4 y[8], xo[8];
; #pragma unroll
;     for (int c = 0; c < 8; ++c) {
;       const uint2 yq = *reinterpret_cast<const uint2*>(yf + (size_t)t * D + c * 256 + lane * 4);
;       y[c] = float4{bflo(yq.x), bfhi(yq.x), bflo(yq.y), bfhi(yq.y)};
;       xo[c] = *reinterpret_cast<const float4*>(p.x + (size_t)t * D + c * 256 + lane * 4);
;     }
.Lgb_wd_13:
.LBB0_1447:
	s_or_b64 exec, exec, s[2:3]
	s_waitcnt lgkmcnt(0)
	s_barrier
	s_and_saveexec_b64 s[2:3], s[6:7]
	s_cbranch_execz .LBB0_1450
	s_load_dwordx4 s[4:7], s[0:1], 0x180
	s_load_dwordx2 s[8:9], s[0:1], 0x230
	v_and_b32_e32 v0, 0xfc, v182
	v_mov_b32_e32 v37, 0
	v_lshlrev_b32_e32 v36, 2, v0
	s_waitcnt lgkmcnt(0)
	v_mov_b32_e32 v2, s4
	v_mov_b32_e32 v3, s5
	s_load_dwordx2 s[2:3], s[0:1], 0x48
	s_load_dwordx2 s[10:11], s[0:1], 0x0
	s_load_dwordx2 s[12:13], s[0:1], 0xd8
	s_load_dwordx2 s[4:5], s[0:1], 0x38
	v_or_b32_e32 v10, 0x400, v0
	s_waitcnt lgkmcnt(0)
	v_lshl_add_u64 v[38:39], s[2:3], 0, v[36:37]
	v_or_b32_e32 v12, 0x500, v0
	v_cmp_lt_i32_e32 vcc, v179, v180
	v_lshl_add_u64 v[40:41], s[4:5], 0, v[36:37]
	v_lshlrev_b32_e32 v36, 2, v10
	v_lshl_add_u64 v[42:43], s[2:3], 0, v[36:37]
	v_lshl_add_u64 v[44:45], s[4:5], 0, v[36:37]
	v_lshlrev_b32_e32 v36, 2, v12
	v_or_b32_e32 v14, 0x600, v0
	v_lshl_add_u64 v[58:59], v[186:187], 2, v[2:3]
	v_lshlrev_b64 v[2:3], 12, v[186:187]
	v_cndmask_b32_e32 v1, v178, v179, vcc
	v_cmp_lt_i32_e32 vcc, v181, v180
	s_lshl_b32 s0, s34, 2
	v_lshl_add_u64 v[46:47], s[2:3], 0, v[36:37]
	v_lshl_add_u64 v[48:49], s[4:5], 0, v[36:37]
	v_lshlrev_b32_e32 v36, 2, v14
	v_or_b32_e32 v16, 0x700, v0
	v_lshl_or_b32 v2, v184, 3, v2
	v_lshlrev_b32_e32 v81, 2, v1
	v_cndmask_b32_e32 v1, v178, v181, vcc
	v_or_b32_e32 v4, 0x100, v0
	v_or_b32_e32 v6, 0x200, v0
	v_or_b32_e32 v8, 0x300, v0
	v_lshl_add_u64 v[50:51], s[2:3], 0, v[36:37]
	v_lshl_add_u64 v[52:53], s[4:5], 0, v[36:37]
	v_lshlrev_b32_e32 v36, 2, v16
	s_ashr_i32 s1, s0, 31
	v_lshl_add_u64 v[60:61], s[8:9], 0, v[2:3]
	v_lshlrev_b64 v[2:3], 13, v[186:187]
	v_lshlrev_b32_e32 v97, 2, v1
	v_lshl_add_u64 v[54:55], s[2:3], 0, v[36:37]
	v_lshl_add_u64 v[56:57], s[4:5], 0, v[36:37]
	s_lshl_b64 s[2:3], s[0:1], 2
	s_lshl_b64 s[4:5], s[0:1], 12
	v_lshl_add_u64 v[62:63], s[12:13], 0, v[2:3]
	s_lshl_b64 s[8:9], s[0:1], 13
	s_waitcnt vmcnt(3)
	v_lshl_add_u64 v[64:65], s[10:11], 0, v[2:3]
	s_mov_b64 s[10:11], 0
	s_mov_b64 s[12:13], 0xa000
	s_mov_b64 s[14:15], 0x4000
	v_lshlrev_b32_e32 v36, 2, v0
	s_waitcnt vmcnt(2)
	v_lshlrev_b32_e32 v66, 2, v4
	s_waitcnt vmcnt(1)
	v_mov_b32_e32 v67, v37
	v_lshlrev_b32_e32 v68, 2, v6
	v_mov_b32_e32 v69, v37
	v_lshlrev_b32_e32 v70, 2, v8
	v_mov_b32_e32 v71, v37
	v_lshlrev_b32_e32 v72, 2, v10
	v_mov_b32_e32 v73, v37
	s_movk_i32 s1, 0x1000
	v_lshlrev_b32_e32 v74, 2, v12
	v_mov_b32_e32 v75, v37
	v_lshlrev_b32_e32 v76, 2, v14
	v_mov_b32_e32 v77, v37
	v_lshlrev_b32_e32 v78, 2, v16
	v_mov_b32_e32 v79, v37
	v_mov_b32_e32 v110, 0x358637bd
	s_mov_b32 s16, 0x800000
	s_movk_i32 s17, 0x1fff
